# 16x16x32 masked-ones row sums combined with the x3-unrolled mixer-B loops (ring offsets as immediates)
# speedup vs baseline: 1.0060x; 1.0002x over previous
; #define ATT_PK4(P, BASE, OUT) do { u32x4 w = {cvtpk(P[BASE + 0], P[BASE + 1]), cvtpk(P[BASE + 2], P[BASE + 3]), cvtpk(P[BASE + 4], P[BASE + 5]), cvtpk(P[BASE + 6], P[BASE + 7])}; \
;     OUT = *reinterpret_cast<bf16x8*>(&w); } while (0)
; template <int DQK> __device__ __forceinline__ void qkt(f32x16& p0, f32x16& p1, const char* Ks, const bf16x8* qr, int r32, int hi) {
;   p0 = f32x16{}; p1 = f32x16{};
; #pragma unroll
;   for (int d0 = 0; d0 < DQK / 16; ++d0) { const int cb = (d0 * 16 + hi * 8) * 2;
;     const bf16x8 b0 = *reinterpret_cast<const bf16x8*>(Ks + kswz<DQK>(r32, cb));
;     const bf16x8 b1 = *reinterpret_cast<const bf16x8*>(Ks + kswz<DQK>(32 + r32, cb));
;     p0 = __builtin_amdgcn_mfma_f32_32x32x16_bf16(b0, qr[d0], p0, 0, 0, 0);
;     p1 = __builtin_amdgcn_mfma_f32_32x32x16_bf16(b1, qr[d0], p1, 0, 0, 0); }
; }
; __device__ __forceinline__ float softmax_shift(f32x16& p0, f32x16& p1, f32x16& negm, float pmax, bool first) {
;   asm volatile("s_nop 4" ::: "memory");
;   { auto rr = __builtin_amdgcn_permlane32_swap(__float_as_uint(pmax), __float_as_uint(pmax), false, false);
;     pmax = fmaxf(__uint_as_float(rr[0]), __uint_as_float(rr[1])); }
;   const float delta = first ? pmax : fmaxf(pmax, 0.f);
; #pragma unroll
;   for (int r = 0; r < 16; ++r) { p0[r] -= delta; p1[r] -= delta; negm[r] -= delta; }
;   return first ? 1.f : __builtin_amdgcn_exp2f(-delta);
; }
; __device__ __forceinline__ void softmax_exp_pack(f32x16& p0, f32x16& p1, bf16x8& pa0, bf16x8& pa1, bf16x8& pa2, bf16x8& pa3) {
; #pragma unroll
;   for (int r = 0; r < 16; ++r) { p0[r] = __builtin_amdgcn_exp2f(p0[r]); p1[r] = __builtin_amdgcn_exp2f(p1[r]); }
;     ...
;   ATT_PK4(p0, 0, pa0); ATT_PK4(p0, 8, pa1); ATT_PK4(p1, 0, pa2); ATT_PK4(p1, 8, pa3);
.LBB0_281:
	v_mul_u32_u24_e32 v18, 0x90, v62
	v_add3_u32 v78, 0, v184, v18
	ds_read_b128 v[18:21], v78 offset:49152
	v_mad_u32_u24 v166, v62, s82, 0
	v_add_u32_e32 v172, v166, v184
	ds_read_b128 v[34:37], v172 offset:53760
	ds_read_b128 v[66:69], v78 offset:49184
	ds_read_b128 v[70:73], v78 offset:49216
	s_and_b32 s4, s92, 0x3fffffc0
	v_and_b32_e32 v63, 63, v63
	s_lshl_b32 s4, s4, 2
	s_add_i32 s6, s4, 0
	s_waitcnt lgkmcnt(3)
	v_mfma_f32_32x32x16_bf16 v[18:33], v[18:21], v[136:139], 0
	s_add_i32 s6, s6, 0x23080
	s_mov_b32 s97, 1
	s_waitcnt lgkmcnt(2)
	v_mfma_f32_32x32x16_bf16 v[34:49], v[34:37], v[136:139], 0
	s_waitcnt lgkmcnt(1)
	v_mfma_f32_32x32x16_bf16 v[18:33], v[66:69], v[140:143], v[18:33]
	ds_read_b128 v[66:69], v78 offset:53792
	ds_read_b128 v[74:77], v78 offset:49248
	s_waitcnt lgkmcnt(1)
	v_mfma_f32_32x32x16_bf16 v[34:49], v[66:69], v[140:143], v[34:49]
	v_mfma_f32_32x32x16_bf16 v[18:33], v[70:73], v[144:147], v[18:33]
	ds_read_b128 v[66:69], v78 offset:53824
	ds_read_b128 v[70:73], v78 offset:53856
	s_waitcnt lgkmcnt(1)
	v_mfma_f32_32x32x16_bf16 v[34:49], v[66:69], v[144:147], v[34:49]
	v_lshlrev_b32_e32 v67, 3, v63
	v_lshlrev_b32_e32 v69, 4, v63
	v_add_u32_e32 v66, 0xc000, v169
	v_and_b32_e32 v68, 24, v67
	v_and_b32_e32 v69, 0xc0, v69
	v_and_b32_e32 v67, 0x100, v67
	v_mfma_f32_32x32x16_bf16 v[18:33], v[74:77], v[148:151], v[18:33]
	v_lshlrev_b32_e32 v74, 1, v63
	v_and_b32_e32 v74, 32, v74
	s_waitcnt lgkmcnt(0)
	v_mfma_f32_32x32x16_bf16 v[34:49], v[70:73], v[148:151], v[34:49]
	s_barrier
	v_cmp_gt_u32_e64 s[4:5], 32, v63
	v_lshl_add_u32 v165, v62, 2, s6
	s_nop 9
	v_add_f32_e32 v62, 0, v34
	v_max3_f32 v63, v62, v18, v19
	v_max3_f32 v63, v63, v20, v21
	v_max3_f32 v63, v63, v22, v23
	v_max3_f32 v63, v63, v24, v25
	v_max3_f32 v63, v63, v26, v27
	v_max3_f32 v63, v63, v28, v29
	v_max3_f32 v63, v63, v30, v31
	v_max3_f32 v63, v63, v32, v33
	s_nop 4
	v_add3_u32 v68, 0, v68, v69
	v_max3_f32 v62, v63, v35, v36
	v_max3_f32 v62, v62, v37, v38
	v_max3_f32 v62, v62, v39, v40
	v_max3_f32 v62, v62, v41, v42
	v_max3_f32 v62, v62, v43, v44
	v_max3_f32 v62, v62, v45, v46
	v_max3_f32 v62, v62, v47, v48
	v_max_f32 v62, v62, v49
	v_add3_u32 v131, v68, v74, v67
	v_mov_b32_e32 v63, v62
	s_nop 1
	v_permlane32_swap_b32_e32 v62, v63
	v_max_f32_e32 v63, v63, v63
	v_max_f32_e32 v62, v62, v62
	v_max_f32_e32 v62, v62, v63
	v_sub_f32_e32 v18, v18, v62
	v_sub_f32_e32 v34, v34, v62
	v_sub_f32_e32 v19, v19, v62
	v_sub_f32_e32 v35, v35, v62
	v_sub_f32_e32 v20, v20, v62
	v_sub_f32_e32 v36, v36, v62
	v_sub_f32_e32 v21, v21, v62
	v_sub_f32_e32 v37, v37, v62
	v_sub_f32_e32 v22, v22, v62
	v_sub_f32_e32 v38, v38, v62
	v_sub_f32_e32 v23, v23, v62
	v_sub_f32_e32 v39, v39, v62
	v_sub_f32_e32 v24, v24, v62
	v_sub_f32_e32 v40, v40, v62
	v_sub_f32_e32 v25, v25, v62
	v_sub_f32_e32 v41, v41, v62
	v_sub_f32_e32 v26, v26, v62
	v_sub_f32_e32 v42, v42, v62
	v_sub_f32_e32 v27, v27, v62
	v_sub_f32_e32 v43, v43, v62
	v_sub_f32_e32 v28, v28, v62
	v_sub_f32_e32 v44, v44, v62
	v_sub_f32_e32 v29, v29, v62
	v_sub_f32_e32 v45, v45, v62
	v_sub_f32_e32 v30, v30, v62
	v_sub_f32_e32 v46, v46, v62
	v_sub_f32_e32 v31, v31, v62
	v_sub_f32_e32 v47, v47, v62
	v_sub_f32_e32 v32, v32, v62
	v_sub_f32_e32 v48, v48, v62
	v_sub_f32_e32 v33, v33, v62
	v_sub_f32_e32 v49, v49, v62
	v_exp_f32_e32 v18, v18
	v_exp_f32_e32 v34, v34
	v_exp_f32_e32 v19, v19
	v_exp_f32_e32 v35, v35
	v_exp_f32_e32 v20, v20
	v_exp_f32_e32 v36, v36
	v_exp_f32_e32 v21, v21
	v_exp_f32_e32 v37, v37
	v_exp_f32_e32 v22, v22
	v_exp_f32_e32 v38, v38
	v_exp_f32_e32 v23, v23
	v_exp_f32_e32 v39, v39
	v_exp_f32_e32 v24, v24
	v_exp_f32_e32 v40, v40
	v_exp_f32_e32 v25, v25
	v_exp_f32_e32 v41, v41
	v_exp_f32_e32 v26, v26
	v_exp_f32_e32 v42, v42
	v_exp_f32_e32 v27, v27
	v_exp_f32_e32 v43, v43
	v_exp_f32_e32 v28, v28
	v_exp_f32_e32 v44, v44
	v_exp_f32_e32 v29, v29
	v_exp_f32_e32 v45, v45
	v_exp_f32_e32 v30, v30
	v_exp_f32_e32 v46, v46
	v_exp_f32_e32 v31, v31
	v_exp_f32_e32 v47, v47
	v_exp_f32_e32 v32, v32
	v_exp_f32_e32 v48, v48
	v_exp_f32_e32 v33, v33
	v_exp_f32_e32 v49, v49
	v_sub_f32_e32 v82, 0, v62
	v_mov_b32_e32 v83, v82
	v_mov_b32_e32 v84, v82
	v_mov_b32_e32 v85, v82
	v_mov_b32_e32 v86, v82
	v_mov_b32_e32 v87, v82
	v_mov_b32_e32 v88, v82
	v_mov_b32_e32 v89, v82
	v_mov_b32_e32 v90, v82
	v_mov_b32_e32 v91, v82
	v_mov_b32_e32 v92, v82
	v_mov_b32_e32 v93, v82
	v_mov_b32_e32 v94, v82
	v_mov_b32_e32 v95, v82
	v_mov_b32_e32 v96, v82
	v_mov_b32_e32 v97, v82
	v_cvt_pk_bf16_f32 v98, v18, v19
	v_cvt_pk_bf16_f32 v99, v20, v21
	v_cvt_pk_bf16_f32 v100, v22, v23
	v_cvt_pk_bf16_f32 v101, v24, v25
	v_cvt_pk_bf16_f32 v102, v26, v27
	v_cvt_pk_bf16_f32 v103, v28, v29
	v_cvt_pk_bf16_f32 v104, v30, v31
	v_cvt_pk_bf16_f32 v105, v32, v33
	v_cvt_pk_bf16_f32 v106, v34, v35
	v_cvt_pk_bf16_f32 v107, v36, v37
	v_cvt_pk_bf16_f32 v108, v38, v39
	v_cvt_pk_bf16_f32 v109, v40, v41
	v_cvt_pk_bf16_f32 v110, v42, v43
	v_cvt_pk_bf16_f32 v111, v44, v45
	v_cvt_pk_bf16_f32 v112, v46, v47
	v_cvt_pk_bf16_f32 v113, v48, v49
	s_waitcnt vmcnt(1)
	ds_write_b128 v66, v[58:61] offset:18432
	ds_write_b128 v64, v[50:53] offset:16384
	s_waitcnt vmcnt(0)
	ds_write_b128 v65, v[54:57] offset:16384
	ds_read_b64_tr_b16 v[18:19], v131
	ds_read_b64_tr_b16 v[20:21], v131 offset:2048
	ds_read_b64_tr_b16 v[34:35], v131 offset:4096
	ds_read_b64_tr_b16 v[36:37], v131 offset:6144
	ds_read_b64_tr_b16 v[38:39], v131 offset:8192
	ds_read_b64_tr_b16 v[40:41], v131 offset:10240
	ds_read_b64_tr_b16 v[42:43], v131 offset:12288
	ds_read_b64_tr_b16 v[44:45], v131 offset:14336
	s_waitcnt lgkmcnt(8)
	s_barrier
; #define ATT_SBAR() __builtin_amdgcn_sched_barrier(0)
; __device__ __forceinline__ unsigned cvtpk(float lo, float hi) { f32x2_t v = {lo, hi}; bf16x2_t b = __builtin_convertvector(v, bf16x2_t); return __builtin_bit_cast(unsigned, b); }
; #define ATT_LOAD_K(t) do { const unsigned so_ = (unsigned)(t) * (unsigned)(KVBLK * LDK * 2); sk0 = __builtin_bit_cast(bf16x8, __builtin_amdgcn_raw_buffer_load_b128(krs, koff, so_, 0)); \
;     if constexpr (DQK == 128) sk1 = __builtin_bit_cast(bf16x8, __builtin_amdgcn_raw_buffer_load_b128(krs, koff, so_ + (unsigned)(32 * LDK * 2), 0)); } while (0)
; #define ATT_LOAD_V(t) do { const unsigned so_ = (unsigned)(t) * (unsigned)(KVBLK * LDV * 2); sv0 = __builtin_bit_cast(bf16x8, __builtin_amdgcn_raw_buffer_load_b128(vrs, voff, so_, 0)); \
;     sv1 = __builtin_bit_cast(bf16x8, __builtin_amdgcn_raw_buffer_load_b128(vrs, voff, so_ + (unsigned)(32 * LDV * 2), 0)); } while (0)
; #define ATT_WRITE_K(so) do { *(bf16x8*)(K_lds + (so) + kswz<DQK>(kr, kc * 2)) = sk0; if constexpr (DQK == 128) *(bf16x8*)(K_lds + (so) + kswz<DQK>(32 + kr, kc * 2)) = sk1; } while (0)
; #define ATT_WRITE_V(so) do { *(bf16x8*)(V_lds + (so) + vst0) = sv0; *(bf16x8*)(V_lds + (so) + vst1) = sv1; } while (0)
;     ...
;   for (int t = 0; t + 1 < NT; ++t) {
;     if constexpr (ABL & 1) { u32x4 w0 = {cvtpk(p0[0], p0[1]), cvtpk(p0[2], p0[3]), cvtpk(p0[4], p0[5]), cvtpk(p0[6], p0[7])}, w1 = {cvtpk(p0[8], p0[9]), cvtpk(p0[10], p0[11]), cvtpk(p0[12], p0[13]), cvtpk(p0[14], p0[15])};
;         u32x4 w2 = {cvtpk(p1[0], p1[1]), cvtpk(p1[2], p1[3]), cvtpk(p1[4], p1[5]), cvtpk(p1[6], p1[7])}, w3 = {cvtpk(p1[8], p1[9]), cvtpk(p1[10], p1[11]), cvtpk(p1[12], p1[13]), cvtpk(p1[14], p1[15])};
;         pa0 = *reinterpret_cast<bf16x8*>(&w0); pa1 = *reinterpret_cast<bf16x8*>(&w1); pa2 = *reinterpret_cast<bf16x8*>(&w2); pa3 = *reinterpret_cast<bf16x8*>(&w3); }
;     else { ATT_SOFTMAX(t == 0); }
;     if constexpr (!(ABL & 4)) { ATT_WRITE_K(k2); ATT_WRITE_V(v1); }
;     ATT_SBAR();
; #pragma unroll
;     for (int ks = 0; ks < 4; ++ks) ATT_VPAIR(va, v0, 0, ks);
;     asm volatile("s_waitcnt lgkmcnt(8)" ::: "memory"); ATT_BAR();
;     ATT_XSECTION(true);
;     if constexpr (!(ABL & 4)) { const int tk = (t + 3 < NT) ? t + 3 : NT - 1, tv = (t + 2 < NT) ? t + 2 : NT - 1; ATT_LOAD_K(tk); ATT_LOAD_V(tv); }
;     ATT_BAR();
	s_setprio 2
	s_waitcnt lgkmcnt(6)
	v_mfma_f32_32x32x16_bf16 v[18:33], v[98:101], v[18:21], 0
	ds_read_b64_tr_b16 v[46:47], v131 offset:512
	ds_read_b64_tr_b16 v[48:49], v131 offset:2560
	s_waitcnt lgkmcnt(6)
	v_mfma_f32_32x32x16_bf16 v[18:33], v[102:105], v[34:37], v[18:33]
	ds_read_b64_tr_b16 v[50:51], v131 offset:4608
	ds_read_b64_tr_b16 v[52:53], v131 offset:6656
	s_waitcnt lgkmcnt(6)
	v_mfma_f32_32x32x16_bf16 v[18:33], v[106:109], v[38:41], v[18:33]
	ds_read_b64_tr_b16 v[54:55], v131 offset:8704
	ds_read_b64_tr_b16 v[56:57], v131 offset:10752
	s_waitcnt lgkmcnt(6)
	v_mfma_f32_32x32x16_bf16 v[18:33], v[110:113], v[42:45], v[18:33]
	ds_read_b64_tr_b16 v[58:59], v131 offset:12800
	ds_read_b64_tr_b16 v[60:61], v131 offset:14848
	s_waitcnt lgkmcnt(6)
	v_mfma_f32_32x32x16_bf16 v[34:49], v[98:101], v[46:49], 0
	ds_read_b64_tr_b16 v[62:63], v131 offset:1024
	ds_read_b64_tr_b16 v[64:65], v131 offset:3072
	s_waitcnt lgkmcnt(6)
	v_mfma_f32_32x32x16_bf16 v[34:49], v[102:105], v[50:53], v[34:49]
	ds_read_b64_tr_b16 v[66:67], v131 offset:5120
	ds_read_b64_tr_b16 v[68:69], v131 offset:7168
	s_waitcnt lgkmcnt(6)
	v_mfma_f32_32x32x16_bf16 v[34:49], v[106:109], v[54:57], v[34:49]
	ds_read_b64_tr_b16 v[70:71], v131 offset:9216
	ds_read_b64_tr_b16 v[72:73], v131 offset:11264
	s_waitcnt lgkmcnt(6)
	v_mfma_f32_32x32x16_bf16 v[34:49], v[110:113], v[58:61], v[34:49]
	ds_read_b64_tr_b16 v[74:75], v131 offset:13312
	ds_read_b64_tr_b16 v[76:77], v131 offset:15360
	s_waitcnt lgkmcnt(6)
	v_mfma_f32_32x32x16_bf16 v[50:65], v[98:101], v[62:65], 0
	ds_read_b64_tr_b16 v[78:79], v131 offset:1536
	ds_read_b64_tr_b16 v[80:81], v131 offset:3584
	s_waitcnt lgkmcnt(6)
	v_mfma_f32_32x32x16_bf16 v[50:65], v[102:105], v[66:69], v[50:65]
	ds_read_b64_tr_b16 v[114:115], v131 offset:5632
	ds_read_b64_tr_b16 v[116:117], v131 offset:7680
	s_waitcnt lgkmcnt(6)
	v_mfma_f32_32x32x16_bf16 v[50:65], v[106:109], v[70:73], v[50:65]
	ds_read_b64_tr_b16 v[118:119], v131 offset:9728
	ds_read_b64_tr_b16 v[120:121], v131 offset:11776
	s_waitcnt lgkmcnt(6)
	v_mfma_f32_32x32x16_bf16 v[50:65], v[110:113], v[74:77], v[50:65]
	ds_read_b64_tr_b16 v[122:123], v131 offset:13824
	ds_read_b64_tr_b16 v[124:125], v131 offset:15872
	s_waitcnt lgkmcnt(6)
	v_mfma_f32_32x32x16_bf16 v[66:81], v[98:101], v[78:81], 0
	ds_read_b128 v[126:129], v172 offset:58368
	s_waitcnt lgkmcnt(5)
	v_mfma_f32_32x32x16_bf16 v[66:81], v[102:105], v[114:117], v[66:81]
	ds_read_b128 v[152:155], v172 offset:62976
	s_waitcnt lgkmcnt(4)
	v_mfma_f32_32x32x16_bf16 v[66:81], v[106:109], v[118:121], v[66:81]
	ds_read_b128 v[156:159], v172 offset:58400
	s_waitcnt lgkmcnt(3)
	v_mfma_f32_32x32x16_bf16 v[66:81], v[110:113], v[122:125], v[66:81]
	ds_read_b128 v[160:163], v172 offset:63008
	v_mfma_f32_16x16x32_bf16 v[240:243], v[98:101], v[132:135], 0
	ds_read_b128 v[174:177], v172 offset:58432
	v_mfma_f32_16x16x32_bf16 v[240:243], v[102:105], v[132:135], v[240:243]
	ds_read_b128 v[178:181], v172 offset:63040
	v_mfma_f32_16x16x32_bf16 v[240:243], v[106:109], v[132:135], v[240:243]
	ds_read_b128 v[186:189], v172 offset:58464
	v_mfma_f32_16x16x32_bf16 v[240:243], v[110:113], v[132:135], v[240:243]
	ds_read_b128 v[190:193], v172 offset:63072
	s_waitcnt lgkmcnt(7)
	v_mfma_f32_32x32x16_bf16 v[98:113], v[126:129], v[136:139], v[82:97]
	v_mov_b64_e32 v[128:129], v[96:97]
	v_mov_b64_e32 v[126:127], v[94:95]
	v_mov_b64_e32 v[124:125], v[92:93]
	v_mov_b64_e32 v[122:123], v[90:91]
	v_mov_b64_e32 v[120:121], v[88:89]
	v_mov_b64_e32 v[118:119], v[86:87]
	v_mov_b64_e32 v[116:117], v[84:85]
	v_mov_b64_e32 v[114:115], v[82:83]
	s_waitcnt lgkmcnt(6)
	s_nop 0
	v_mfma_f32_32x32x16_bf16 v[114:129], v[152:155], v[136:139], v[114:129]
	s_waitcnt lgkmcnt(5)
	v_mfma_f32_32x32x16_bf16 v[98:113], v[156:159], v[140:143], v[98:113]
	s_waitcnt lgkmcnt(4)
	v_mfma_f32_32x32x16_bf16 v[114:129], v[160:163], v[140:143], v[114:129]
	s_waitcnt lgkmcnt(3)
	v_mfma_f32_32x32x16_bf16 v[98:113], v[174:177], v[144:147], v[98:113]
	s_waitcnt lgkmcnt(2)
	v_mfma_f32_32x32x16_bf16 v[114:129], v[178:181], v[144:147], v[114:129]
	s_waitcnt lgkmcnt(1)
	v_mfma_f32_32x32x16_bf16 v[98:113], v[186:189], v[148:151], v[98:113]
	s_waitcnt lgkmcnt(0)
	v_mfma_f32_32x32x16_bf16 v[114:129], v[190:193], v[148:151], v[114:129]
	s_setprio 0
	s_mov_b32 s14, s10
	s_mov_b32 s15, s11
	buffer_load_dwordx4 v[224:227], v170, s[8:11], s85 offen
	buffer_load_dwordx4 v[228:231], v171, s[12:15], s83 offen
	buffer_load_dwordx4 v[232:235], v171, s[12:15], s86 offen
	s_barrier
	s_mov_b32 s95, 0x8000
	s_movk_i32 s15, 0x4000
	s_movk_i32 s18, 0x2400
	s_mov_b32 s94, 0
	s_movk_i32 s14, 0x4800
	s_mov_b32 s36, 0x70000
	s_mov_b32 s93, 0
	v_add_f32_e32 v173, 0, v114
	v_max3_f32 v174, v173, v98, v99
	v_max3_f32 v174, v174, v100, v101
	v_max3_f32 v174, v174, v102, v103
	v_max3_f32 v174, v174, v104, v105
	v_max3_f32 v174, v174, v106, v107
	v_max3_f32 v174, v174, v108, v109
	v_max3_f32 v174, v174, v110, v111
	v_max3_f32 v174, v174, v112, v113
	v_max3_f32 v173, v174, v115, v116
	v_max3_f32 v173, v173, v117, v118
	v_max3_f32 v173, v173, v119, v120
	v_max3_f32 v173, v173, v121, v122
	v_max3_f32 v173, v173, v123, v124
	v_max3_f32 v173, v173, v125, v126
	v_max3_f32 v173, v173, v127, v128
	v_max_f32 v173, v173, v129
	v_add_u32_e32 v248, 0x8000, v169
	v_add_u32_e32 v249, 0x8000, v172

; #define ATT_SBAR() __builtin_amdgcn_sched_barrier(0)
; __device__ __forceinline__ unsigned cvtpk(float lo, float hi) { f32x2_t v = {lo, hi}; bf16x2_t b = __builtin_convertvector(v, bf16x2_t); return __builtin_bit_cast(unsigned, b); }
; #define ATT_LOAD_K(t) do { const unsigned so_ = (unsigned)(t) * (unsigned)(KVBLK * LDK * 2); sk0 = __builtin_bit_cast(bf16x8, __builtin_amdgcn_raw_buffer_load_b128(krs, koff, so_, 0)); \
;     if constexpr (DQK == 128) sk1 = __builtin_bit_cast(bf16x8, __builtin_amdgcn_raw_buffer_load_b128(krs, koff, so_ + (unsigned)(32 * LDK * 2), 0)); } while (0)
; #define ATT_LOAD_V(t) do { const unsigned so_ = (unsigned)(t) * (unsigned)(KVBLK * LDV * 2); sv0 = __builtin_bit_cast(bf16x8, __builtin_amdgcn_raw_buffer_load_b128(vrs, voff, so_, 0)); \
;     sv1 = __builtin_bit_cast(bf16x8, __builtin_amdgcn_raw_buffer_load_b128(vrs, voff, so_ + (unsigned)(32 * LDV * 2), 0)); } while (0)
; #define ATT_WRITE_K(so) do { *(bf16x8*)(K_lds + (so) + kswz<DQK>(kr, kc * 2)) = sk0; if constexpr (DQK == 128) *(bf16x8*)(K_lds + (so) + kswz<DQK>(32 + kr, kc * 2)) = sk1; } while (0)
;     ...
;   for (int t = 0; t + 1 < NT; ++t) {
;     if constexpr (ABL & 1) { u32x4 w0 = {cvtpk(p0[0], p0[1]), cvtpk(p0[2], p0[3]), cvtpk(p0[4], p0[5]), cvtpk(p0[6], p0[7])}, w1 = {cvtpk(p0[8], p0[9]), cvtpk(p0[10], p0[11]), cvtpk(p0[12], p0[13]), cvtpk(p0[14], p0[15])};
;         u32x4 w2 = {cvtpk(p1[0], p1[1]), cvtpk(p1[2], p1[3]), cvtpk(p1[4], p1[5]), cvtpk(p1[6], p1[7])}, w3 = {cvtpk(p1[8], p1[9]), cvtpk(p1[10], p1[11]), cvtpk(p1[12], p1[13]), cvtpk(p1[14], p1[15])};
;         pa0 = *reinterpret_cast<bf16x8*>(&w0); pa1 = *reinterpret_cast<bf16x8*>(&w1); pa2 = *reinterpret_cast<bf16x8*>(&w2); pa3 = *reinterpret_cast<bf16x8*>(&w3); }
;     else { ATT_SOFTMAX(t == 0); }
;     if constexpr (!(ABL & 4)) { ATT_WRITE_K(k2); ATT_WRITE_V(v1); }
;     ATT_SBAR();
; #pragma unroll
;     for (int ks = 0; ks < 4; ++ks) ATT_VPAIR(va, v0, 0, ks);
;     asm volatile("s_waitcnt lgkmcnt(8)" ::: "memory"); ATT_BAR();
;     ATT_XSECTION(true);
;     if constexpr (!(ABL & 4)) { const int tk = (t + 3 < NT) ? t + 3 : NT - 1, tv = (t + 2 < NT) ? t + 2 : NT - 1; ATT_LOAD_K(tk); ATT_LOAD_V(tv); }
;     ATT_BAR();
;     { const int tk_ = k0; k0 = k1; k1 = k2; k2 = tk_; const int tv_ = v0; v0 = v1; v1 = v2; v2 = tv_; }
.LBB0_283:
	v_exp_f32_e32 v98, v98
	v_exp_f32_e32 v114, v114
	v_exp_f32_e32 v99, v99
	v_exp_f32_e32 v115, v115
	v_exp_f32_e32 v100, v100
	v_exp_f32_e32 v101, v101
	v_exp_f32_e32 v102, v102
	v_exp_f32_e32 v103, v103
	v_exp_f32_e32 v106, v106
	v_exp_f32_e32 v107, v107
	v_exp_f32_e32 v116, v116
	v_exp_f32_e32 v117, v117
	v_exp_f32_e32 v118, v118
	v_exp_f32_e32 v119, v119
	v_exp_f32_e32 v104, v104
	v_exp_f32_e32 v120, v120
	v_exp_f32_e32 v105, v105
	v_exp_f32_e32 v121, v121
	v_exp_f32_e32 v122, v122
	v_exp_f32_e32 v123, v123
	v_exp_f32_e32 v108, v108
	v_exp_f32_e32 v124, v124
	v_exp_f32_e32 v109, v109
	v_exp_f32_e32 v125, v125
	v_exp_f32_e32 v110, v110
	v_exp_f32_e32 v126, v126
	v_exp_f32_e32 v111, v111
	v_exp_f32_e32 v127, v127
	v_exp_f32_e32 v112, v112
	v_exp_f32_e32 v128, v128
	v_exp_f32_e32 v113, v113
	v_exp_f32_e32 v129, v129
	v_cvt_pk_bf16_f32 v2, v98, v99
	v_cvt_pk_bf16_f32 v3, v100, v101
	v_cvt_pk_bf16_f32 v4, v102, v103
	v_cvt_pk_bf16_f32 v6, v106, v107
	v_cvt_pk_bf16_f32 v10, v114, v115
	v_cvt_pk_bf16_f32 v5, v104, v105
	v_cvt_pk_bf16_f32 v7, v108, v109
	v_cvt_pk_bf16_f32 v8, v110, v111
	v_cvt_pk_bf16_f32 v9, v112, v113
	v_cvt_pk_bf16_f32 v11, v116, v117
	v_cvt_pk_bf16_f32 v12, v118, v119
	v_cvt_pk_bf16_f32 v13, v120, v121
	v_cvt_pk_bf16_f32 v14, v122, v123
	v_cvt_pk_bf16_f32 v15, v124, v125
	v_cvt_pk_bf16_f32 v16, v126, v127
	v_cvt_pk_bf16_f32 v17, v128, v129
	s_waitcnt vmcnt(0)
	ds_write_b128 v248, v[224:227] offset:16384
	ds_write_b128 v167, v[228:231] offset:32768
	ds_write_b128 v168, v[232:235] offset:32768
	ds_read_b128 v[152:155], v249 offset:34816
	ds_read_b128 v[156:159], v249 offset:39424
	ds_read_b128 v[160:163], v249 offset:34848
	ds_read_b128 v[176:179], v249 offset:39456
	s_waitcnt lgkmcnt(4)
	s_barrier
	s_setprio 2
	s_waitcnt lgkmcnt(3)
	v_mfma_f32_32x32x16_bf16 v[98:113], v[152:155], v[136:139], v[82:97]
	ds_read_b128 v[180:183], v249 offset:34880
	s_waitcnt lgkmcnt(3)
	v_mfma_f32_32x32x16_bf16 v[114:129], v[156:159], v[136:139], v[82:97]
	ds_read_b128 v[186:189], v249 offset:39488
	s_waitcnt lgkmcnt(3)
	v_mfma_f32_32x32x16_bf16 v[98:113], v[160:163], v[140:143], v[98:113]
	ds_read_b128 v[190:193], v249 offset:34912
	ds_read_b64_tr_b16 v[198:199], v131 offset:16384
	ds_read_b64_tr_b16 v[200:201], v131 offset:18432
	s_waitcnt lgkmcnt(5)
	v_mfma_f32_32x32x16_bf16 v[114:129], v[176:179], v[140:143], v[114:129]
	ds_read_b128 v[194:197], v249 offset:39520
	ds_read_b64_tr_b16 v[212:213], v131 offset:20480
	ds_read_b64_tr_b16 v[214:215], v131 offset:22528
	s_waitcnt lgkmcnt(7)
	v_mfma_f32_32x32x16_bf16 v[98:113], v[180:183], v[144:147], v[98:113]
	ds_read_b64_tr_b16 v[216:217], v131 offset:24576
	ds_read_b64_tr_b16 v[218:219], v131 offset:26624
	s_waitcnt lgkmcnt(8)
	v_mfma_f32_32x32x16_bf16 v[114:129], v[186:189], v[144:147], v[114:129]
	ds_read_b64_tr_b16 v[220:221], v131 offset:28672
	ds_read_b64_tr_b16 v[222:223], v131 offset:30720
	s_waitcnt lgkmcnt(9)
	v_mfma_f32_32x32x16_bf16 v[98:113], v[190:193], v[148:151], v[98:113]
	s_waitcnt lgkmcnt(6)
	v_mfma_f32_32x32x16_bf16 v[114:129], v[194:197], v[148:151], v[114:129]
	v_mfma_f32_32x32x16_bf16 v[18:33], v[2:5], v[198:201], v[18:33]
	ds_read_b64_tr_b16 v[236:237], v131 offset:16896
	ds_read_b64_tr_b16 v[238:239], v131 offset:18944
	s_waitcnt lgkmcnt(6)
	v_mfma_f32_32x32x16_bf16 v[18:33], v[6:9], v[212:215], v[18:33]
	ds_read_b64_tr_b16 v[198:199], v131 offset:20992
	ds_read_b64_tr_b16 v[200:201], v131 offset:23040
	s_waitcnt lgkmcnt(6)
	v_mfma_f32_32x32x16_bf16 v[18:33], v[10:13], v[216:219], v[18:33]
	ds_read_b64_tr_b16 v[212:213], v131 offset:25088
	ds_read_b64_tr_b16 v[214:215], v131 offset:27136
	s_waitcnt lgkmcnt(6)
	v_mfma_f32_32x32x16_bf16 v[18:33], v[14:17], v[220:223], v[18:33]
	ds_read_b64_tr_b16 v[216:217], v131 offset:29184
	ds_read_b64_tr_b16 v[218:219], v131 offset:31232
	v_max3_f32 v152, v98, v99, v100
	s_waitcnt lgkmcnt(6)
	v_mfma_f32_32x32x16_bf16 v[34:49], v[2:5], v[236:239], v[34:49]
	ds_read_b64_tr_b16 v[220:221], v131 offset:17408
	ds_read_b64_tr_b16 v[222:223], v131 offset:19456
	v_max3_f32 v173, v114, v115, v116
	s_waitcnt lgkmcnt(6)
	v_mfma_f32_32x32x16_bf16 v[34:49], v[6:9], v[198:201], v[34:49]
	ds_read_b64_tr_b16 v[236:237], v131 offset:21504
	ds_read_b64_tr_b16 v[238:239], v131 offset:23552
	v_max3_f32 v152, v152, v101, v102
	s_waitcnt lgkmcnt(6)
	v_mfma_f32_32x32x16_bf16 v[34:49], v[10:13], v[212:215], v[34:49]
	ds_read_b64_tr_b16 v[198:199], v131 offset:25600
	ds_read_b64_tr_b16 v[200:201], v131 offset:27648
	v_max3_f32 v173, v173, v117, v118
	s_waitcnt lgkmcnt(6)
	v_mfma_f32_32x32x16_bf16 v[34:49], v[14:17], v[216:219], v[34:49]
	ds_read_b64_tr_b16 v[212:213], v131 offset:29696
	ds_read_b64_tr_b16 v[214:215], v131 offset:31744
	v_max3_f32 v152, v152, v103, v104
	s_waitcnt lgkmcnt(6)
	v_mfma_f32_32x32x16_bf16 v[50:65], v[2:5], v[220:223], v[50:65]
	ds_read_b64_tr_b16 v[216:217], v131 offset:17920
	ds_read_b64_tr_b16 v[218:219], v131 offset:19968
	v_max3_f32 v173, v173, v119, v120
	s_waitcnt lgkmcnt(6)
	v_mfma_f32_32x32x16_bf16 v[50:65], v[6:9], v[236:239], v[50:65]
	ds_read_b64_tr_b16 v[220:221], v131 offset:22016
	ds_read_b64_tr_b16 v[222:223], v131 offset:24064
	v_max3_f32 v152, v152, v105, v106
	s_waitcnt lgkmcnt(6)
	v_mfma_f32_32x32x16_bf16 v[50:65], v[10:13], v[198:201], v[50:65]
	ds_read_b64_tr_b16 v[236:237], v131 offset:26112
	ds_read_b64_tr_b16 v[238:239], v131 offset:28160
	v_max3_f32 v173, v173, v121, v122
	s_waitcnt lgkmcnt(6)
	v_mfma_f32_32x32x16_bf16 v[50:65], v[14:17], v[212:215], v[50:65]
	ds_read_b64_tr_b16 v[198:199], v131 offset:30208
	ds_read_b64_tr_b16 v[200:201], v131 offset:32256
	v_max3_f32 v152, v152, v107, v108
	s_waitcnt lgkmcnt(6)
	v_mfma_f32_32x32x16_bf16 v[66:81], v[2:5], v[216:219], v[66:81]
	v_max3_f32 v173, v173, v123, v124
	s_min_u32 s14, s97, 0x7c
	s_lshl_b32 s14, s14, 17
	s_add_i32 s14, s14, 0x60000
	buffer_load_dwordx4 v[224:227], v170, s[8:11], s14 offen
	s_waitcnt lgkmcnt(4)
	v_mfma_f32_32x32x16_bf16 v[66:81], v[6:9], v[220:223], v[66:81]
	v_max3_f32 v152, v152, v109, v110
	s_add_i32 s19, s36, 0xffff0000
	s_mov_b32 s14, s10
	s_mov_b32 s15, s11
	buffer_load_dwordx4 v[228:231], v171, s[12:15], s19 offen
	s_waitcnt lgkmcnt(2)
	v_mfma_f32_32x32x16_bf16 v[66:81], v[10:13], v[236:239], v[66:81]
	v_max3_f32 v173, v173, v125, v126
	buffer_load_dwordx4 v[232:235], v171, s[12:15], s36 offen
	s_waitcnt lgkmcnt(0)
	v_mfma_f32_32x32x16_bf16 v[66:81], v[14:17], v[198:201], v[66:81]
	v_max3_f32 v152, v152, v111, v112
	v_mfma_f32_16x16x32_bf16 v[240:243], v[2:5], v[132:135], v[240:243]
	v_max3_f32 v173, v173, v127, v128
	v_mfma_f32_16x16x32_bf16 v[240:243], v[6:9], v[132:135], v[240:243]
	v_max_f32 v152, v152, v113
	v_mfma_f32_16x16x32_bf16 v[240:243], v[10:13], v[132:135], v[240:243]
	v_max_f32 v173, v173, v129
	v_mfma_f32_16x16x32_bf16 v[240:243], v[14:17], v[132:135], v[240:243]
	v_max_f32 v173, v173, v152
	s_setprio 0
	s_barrier
	s_add_i32 s36, s36, 0x20000
	s_add_i32 s97, s97, 1
	s_cmpk_eq_i32 s97, 0x7e
	s_cbranch_scc1 .Lu3_exit_b1_0

; #define ATT_SBAR() __builtin_amdgcn_sched_barrier(0)
; __device__ __forceinline__ unsigned cvtpk(float lo, float hi) { f32x2_t v = {lo, hi}; bf16x2_t b = __builtin_convertvector(v, bf16x2_t); return __builtin_bit_cast(unsigned, b); }
; #define ATT_LOAD_K(t) do { const unsigned so_ = (unsigned)(t) * (unsigned)(KVBLK * LDK * 2); sk0 = __builtin_bit_cast(bf16x8, __builtin_amdgcn_raw_buffer_load_b128(krs, koff, so_, 0)); \
;     if constexpr (DQK == 128) sk1 = __builtin_bit_cast(bf16x8, __builtin_amdgcn_raw_buffer_load_b128(krs, koff, so_ + (unsigned)(32 * LDK * 2), 0)); } while (0)
; #define ATT_LOAD_V(t) do { const unsigned so_ = (unsigned)(t) * (unsigned)(KVBLK * LDV * 2); sv0 = __builtin_bit_cast(bf16x8, __builtin_amdgcn_raw_buffer_load_b128(vrs, voff, so_, 0)); \
;     sv1 = __builtin_bit_cast(bf16x8, __builtin_amdgcn_raw_buffer_load_b128(vrs, voff, so_ + (unsigned)(32 * LDV * 2), 0)); } while (0)
; #define ATT_WRITE_K(so) do { *(bf16x8*)(K_lds + (so) + kswz<DQK>(kr, kc * 2)) = sk0; if constexpr (DQK == 128) *(bf16x8*)(K_lds + (so) + kswz<DQK>(32 + kr, kc * 2)) = sk1; } while (0)
;     ...
;   for (int t = 0; t + 1 < NT; ++t) {
;     if constexpr (ABL & 1) { u32x4 w0 = {cvtpk(p0[0], p0[1]), cvtpk(p0[2], p0[3]), cvtpk(p0[4], p0[5]), cvtpk(p0[6], p0[7])}, w1 = {cvtpk(p0[8], p0[9]), cvtpk(p0[10], p0[11]), cvtpk(p0[12], p0[13]), cvtpk(p0[14], p0[15])};
;         u32x4 w2 = {cvtpk(p1[0], p1[1]), cvtpk(p1[2], p1[3]), cvtpk(p1[4], p1[5]), cvtpk(p1[6], p1[7])}, w3 = {cvtpk(p1[8], p1[9]), cvtpk(p1[10], p1[11]), cvtpk(p1[12], p1[13]), cvtpk(p1[14], p1[15])};
;         pa0 = *reinterpret_cast<bf16x8*>(&w0); pa1 = *reinterpret_cast<bf16x8*>(&w1); pa2 = *reinterpret_cast<bf16x8*>(&w2); pa3 = *reinterpret_cast<bf16x8*>(&w3); }
;     else { ATT_SOFTMAX(t == 0); }
;     if constexpr (!(ABL & 4)) { ATT_WRITE_K(k2); ATT_WRITE_V(v1); }
;     ATT_SBAR();
; #pragma unroll
;     for (int ks = 0; ks < 4; ++ks) ATT_VPAIR(va, v0, 0, ks);
;     asm volatile("s_waitcnt lgkmcnt(8)" ::: "memory"); ATT_BAR();
;     ATT_XSECTION(true);
;     if constexpr (!(ABL & 4)) { const int tk = (t + 3 < NT) ? t + 3 : NT - 1, tv = (t + 2 < NT) ? t + 2 : NT - 1; ATT_LOAD_K(tk); ATT_LOAD_V(tv); }
;     ATT_BAR();
;     { const int tk_ = k0; k0 = k1; k1 = k2; k2 = tk_; const int tv_ = v0; v0 = v1; v1 = v2; v2 = tv_; }
.Lu3_join_b1_1:
	v_exp_f32_e32 v98, v98
	v_exp_f32_e32 v114, v114
	v_exp_f32_e32 v99, v99
	v_exp_f32_e32 v115, v115
	v_exp_f32_e32 v100, v100
	v_exp_f32_e32 v101, v101
	v_exp_f32_e32 v102, v102
	v_exp_f32_e32 v103, v103
	v_exp_f32_e32 v106, v106
	v_exp_f32_e32 v107, v107
	v_exp_f32_e32 v116, v116
	v_exp_f32_e32 v117, v117
	v_exp_f32_e32 v118, v118
	v_exp_f32_e32 v119, v119
	v_exp_f32_e32 v104, v104
	v_exp_f32_e32 v120, v120
	v_exp_f32_e32 v105, v105
	v_exp_f32_e32 v121, v121
	v_exp_f32_e32 v122, v122
	v_exp_f32_e32 v123, v123
	v_exp_f32_e32 v108, v108
	v_exp_f32_e32 v124, v124
	v_exp_f32_e32 v109, v109
	v_exp_f32_e32 v125, v125
	v_exp_f32_e32 v110, v110
	v_exp_f32_e32 v126, v126
	v_exp_f32_e32 v111, v111
	v_exp_f32_e32 v127, v127
	v_exp_f32_e32 v112, v112
	v_exp_f32_e32 v128, v128
	v_exp_f32_e32 v113, v113
	v_exp_f32_e32 v129, v129
	v_cvt_pk_bf16_f32 v2, v98, v99
	v_cvt_pk_bf16_f32 v3, v100, v101
	v_cvt_pk_bf16_f32 v4, v102, v103
	v_cvt_pk_bf16_f32 v6, v106, v107
	v_cvt_pk_bf16_f32 v10, v114, v115
	v_cvt_pk_bf16_f32 v5, v104, v105
	v_cvt_pk_bf16_f32 v7, v108, v109
	v_cvt_pk_bf16_f32 v8, v110, v111
	v_cvt_pk_bf16_f32 v9, v112, v113
	v_cvt_pk_bf16_f32 v11, v116, v117
	v_cvt_pk_bf16_f32 v12, v118, v119
	v_cvt_pk_bf16_f32 v13, v120, v121
	v_cvt_pk_bf16_f32 v14, v122, v123
	v_cvt_pk_bf16_f32 v15, v124, v125
	v_cvt_pk_bf16_f32 v16, v126, v127
	v_cvt_pk_bf16_f32 v17, v128, v129
	s_waitcnt vmcnt(0)
	ds_write_b128 v248, v[224:227] offset:25600
	ds_write_b128 v167, v[228:231]
	ds_write_b128 v168, v[232:235]
	ds_read_b128 v[152:155], v249 offset:16384
	ds_read_b128 v[156:159], v249 offset:20992
	ds_read_b128 v[160:163], v249 offset:16416
	ds_read_b128 v[176:179], v249 offset:21024
	s_waitcnt lgkmcnt(4)
	s_barrier
	s_setprio 2
	s_waitcnt lgkmcnt(3)
	v_mfma_f32_32x32x16_bf16 v[98:113], v[152:155], v[136:139], v[82:97]
	ds_read_b128 v[180:183], v249 offset:16448
	s_waitcnt lgkmcnt(3)
	v_mfma_f32_32x32x16_bf16 v[114:129], v[156:159], v[136:139], v[82:97]
	ds_read_b128 v[186:189], v249 offset:21056
	s_waitcnt lgkmcnt(3)
	v_mfma_f32_32x32x16_bf16 v[98:113], v[160:163], v[140:143], v[98:113]
	ds_read_b128 v[190:193], v249 offset:16480
	ds_read_b64_tr_b16 v[198:199], v131 offset:32768
	ds_read_b64_tr_b16 v[200:201], v131 offset:34816
	s_waitcnt lgkmcnt(5)
	v_mfma_f32_32x32x16_bf16 v[114:129], v[176:179], v[140:143], v[114:129]
	ds_read_b128 v[194:197], v249 offset:21088
	ds_read_b64_tr_b16 v[212:213], v131 offset:36864
	ds_read_b64_tr_b16 v[214:215], v131 offset:38912
	s_waitcnt lgkmcnt(7)
	v_mfma_f32_32x32x16_bf16 v[98:113], v[180:183], v[144:147], v[98:113]
	ds_read_b64_tr_b16 v[216:217], v131 offset:40960
	ds_read_b64_tr_b16 v[218:219], v131 offset:43008
	s_waitcnt lgkmcnt(8)
	v_mfma_f32_32x32x16_bf16 v[114:129], v[186:189], v[144:147], v[114:129]
	ds_read_b64_tr_b16 v[220:221], v131 offset:45056
	ds_read_b64_tr_b16 v[222:223], v131 offset:47104
	s_waitcnt lgkmcnt(9)
	v_mfma_f32_32x32x16_bf16 v[98:113], v[190:193], v[148:151], v[98:113]
	s_waitcnt lgkmcnt(6)
	v_mfma_f32_32x32x16_bf16 v[114:129], v[194:197], v[148:151], v[114:129]
	v_mfma_f32_32x32x16_bf16 v[18:33], v[2:5], v[198:201], v[18:33]
	ds_read_b64_tr_b16 v[236:237], v131 offset:33280
	ds_read_b64_tr_b16 v[238:239], v131 offset:35328
	s_waitcnt lgkmcnt(6)
	v_mfma_f32_32x32x16_bf16 v[18:33], v[6:9], v[212:215], v[18:33]
	ds_read_b64_tr_b16 v[198:199], v131 offset:37376
	ds_read_b64_tr_b16 v[200:201], v131 offset:39424
	s_waitcnt lgkmcnt(6)
	v_mfma_f32_32x32x16_bf16 v[18:33], v[10:13], v[216:219], v[18:33]
	ds_read_b64_tr_b16 v[212:213], v131 offset:41472
	ds_read_b64_tr_b16 v[214:215], v131 offset:43520
	s_waitcnt lgkmcnt(6)
	v_mfma_f32_32x32x16_bf16 v[18:33], v[14:17], v[220:223], v[18:33]
	ds_read_b64_tr_b16 v[216:217], v131 offset:45568
	ds_read_b64_tr_b16 v[218:219], v131 offset:47616
	v_max3_f32 v152, v98, v99, v100
	s_waitcnt lgkmcnt(6)
	v_mfma_f32_32x32x16_bf16 v[34:49], v[2:5], v[236:239], v[34:49]
	ds_read_b64_tr_b16 v[220:221], v131 offset:33792
	ds_read_b64_tr_b16 v[222:223], v131 offset:35840
	v_max3_f32 v173, v114, v115, v116
	s_waitcnt lgkmcnt(6)
	v_mfma_f32_32x32x16_bf16 v[34:49], v[6:9], v[198:201], v[34:49]
	ds_read_b64_tr_b16 v[236:237], v131 offset:37888
	ds_read_b64_tr_b16 v[238:239], v131 offset:39936
	v_max3_f32 v152, v152, v101, v102
	s_waitcnt lgkmcnt(6)
	v_mfma_f32_32x32x16_bf16 v[34:49], v[10:13], v[212:215], v[34:49]
	ds_read_b64_tr_b16 v[198:199], v131 offset:41984
	ds_read_b64_tr_b16 v[200:201], v131 offset:44032
	v_max3_f32 v173, v173, v117, v118
	s_waitcnt lgkmcnt(6)
	v_mfma_f32_32x32x16_bf16 v[34:49], v[14:17], v[216:219], v[34:49]
	ds_read_b64_tr_b16 v[212:213], v131 offset:46080
	ds_read_b64_tr_b16 v[214:215], v131 offset:48128
	v_max3_f32 v152, v152, v103, v104
	s_waitcnt lgkmcnt(6)
	v_mfma_f32_32x32x16_bf16 v[50:65], v[2:5], v[220:223], v[50:65]
	ds_read_b64_tr_b16 v[216:217], v131 offset:34304
	ds_read_b64_tr_b16 v[218:219], v131 offset:36352
	v_max3_f32 v173, v173, v119, v120
	s_waitcnt lgkmcnt(6)
	v_mfma_f32_32x32x16_bf16 v[50:65], v[6:9], v[236:239], v[50:65]
	ds_read_b64_tr_b16 v[220:221], v131 offset:38400
	ds_read_b64_tr_b16 v[222:223], v131 offset:40448
	v_max3_f32 v152, v152, v105, v106
	s_waitcnt lgkmcnt(6)
	v_mfma_f32_32x32x16_bf16 v[50:65], v[10:13], v[198:201], v[50:65]
	ds_read_b64_tr_b16 v[236:237], v131 offset:42496
	ds_read_b64_tr_b16 v[238:239], v131 offset:44544
	v_max3_f32 v173, v173, v121, v122
	s_waitcnt lgkmcnt(6)
	v_mfma_f32_32x32x16_bf16 v[50:65], v[14:17], v[212:215], v[50:65]
	ds_read_b64_tr_b16 v[198:199], v131 offset:46592
	ds_read_b64_tr_b16 v[200:201], v131 offset:48640
	v_max3_f32 v152, v152, v107, v108
	s_waitcnt lgkmcnt(6)
	v_mfma_f32_32x32x16_bf16 v[66:81], v[2:5], v[216:219], v[66:81]
	v_max3_f32 v173, v173, v123, v124
	s_min_u32 s14, s97, 0x7c
	s_lshl_b32 s14, s14, 17
	s_add_i32 s14, s14, 0x60000
	buffer_load_dwordx4 v[224:227], v170, s[8:11], s14 offen
	s_waitcnt lgkmcnt(4)
	v_mfma_f32_32x32x16_bf16 v[66:81], v[6:9], v[220:223], v[66:81]
	v_max3_f32 v152, v152, v109, v110
	s_add_i32 s19, s36, 0xffff0000
	s_mov_b32 s14, s10
	s_mov_b32 s15, s11
	buffer_load_dwordx4 v[228:231], v171, s[12:15], s19 offen
	s_waitcnt lgkmcnt(2)
	v_mfma_f32_32x32x16_bf16 v[66:81], v[10:13], v[236:239], v[66:81]
	v_max3_f32 v173, v173, v125, v126
	buffer_load_dwordx4 v[232:235], v171, s[12:15], s36 offen
	s_waitcnt lgkmcnt(0)
	v_mfma_f32_32x32x16_bf16 v[66:81], v[14:17], v[198:201], v[66:81]
	v_max3_f32 v152, v152, v111, v112
	v_mfma_f32_16x16x32_bf16 v[240:243], v[2:5], v[132:135], v[240:243]
	v_max3_f32 v173, v173, v127, v128
	v_mfma_f32_16x16x32_bf16 v[240:243], v[6:9], v[132:135], v[240:243]
	v_max_f32 v152, v152, v113
	v_mfma_f32_16x16x32_bf16 v[240:243], v[10:13], v[132:135], v[240:243]
	v_max_f32 v173, v173, v129
	v_mfma_f32_16x16x32_bf16 v[240:243], v[14:17], v[132:135], v[240:243]
	v_max_f32 v173, v173, v152
	s_setprio 0
	s_barrier
	s_add_i32 s36, s36, 0x20000
	s_add_i32 s97, s97, 1
	s_cmpk_eq_i32 s97, 0x7e
	s_cbranch_scc1 .Lu3_exit_b1_1

; #define ATT_SBAR() __builtin_amdgcn_sched_barrier(0)
; __device__ __forceinline__ unsigned cvtpk(float lo, float hi) { f32x2_t v = {lo, hi}; bf16x2_t b = __builtin_convertvector(v, bf16x2_t); return __builtin_bit_cast(unsigned, b); }
; #define ATT_LOAD_K(t) do { const unsigned so_ = (unsigned)(t) * (unsigned)(KVBLK * LDK * 2); sk0 = __builtin_bit_cast(bf16x8, __builtin_amdgcn_raw_buffer_load_b128(krs, koff, so_, 0)); \
;     if constexpr (DQK == 128) sk1 = __builtin_bit_cast(bf16x8, __builtin_amdgcn_raw_buffer_load_b128(krs, koff, so_ + (unsigned)(32 * LDK * 2), 0)); } while (0)
; #define ATT_LOAD_V(t) do { const unsigned so_ = (unsigned)(t) * (unsigned)(KVBLK * LDV * 2); sv0 = __builtin_bit_cast(bf16x8, __builtin_amdgcn_raw_buffer_load_b128(vrs, voff, so_, 0)); \
;     sv1 = __builtin_bit_cast(bf16x8, __builtin_amdgcn_raw_buffer_load_b128(vrs, voff, so_ + (unsigned)(32 * LDV * 2), 0)); } while (0)
; #define ATT_WRITE_K(so) do { *(bf16x8*)(K_lds + (so) + kswz<DQK>(kr, kc * 2)) = sk0; if constexpr (DQK == 128) *(bf16x8*)(K_lds + (so) + kswz<DQK>(32 + kr, kc * 2)) = sk1; } while (0)
;     ...
;   for (int t = 0; t + 1 < NT; ++t) {
;     if constexpr (ABL & 1) { u32x4 w0 = {cvtpk(p0[0], p0[1]), cvtpk(p0[2], p0[3]), cvtpk(p0[4], p0[5]), cvtpk(p0[6], p0[7])}, w1 = {cvtpk(p0[8], p0[9]), cvtpk(p0[10], p0[11]), cvtpk(p0[12], p0[13]), cvtpk(p0[14], p0[15])};
;         u32x4 w2 = {cvtpk(p1[0], p1[1]), cvtpk(p1[2], p1[3]), cvtpk(p1[4], p1[5]), cvtpk(p1[6], p1[7])}, w3 = {cvtpk(p1[8], p1[9]), cvtpk(p1[10], p1[11]), cvtpk(p1[12], p1[13]), cvtpk(p1[14], p1[15])};
;         pa0 = *reinterpret_cast<bf16x8*>(&w0); pa1 = *reinterpret_cast<bf16x8*>(&w1); pa2 = *reinterpret_cast<bf16x8*>(&w2); pa3 = *reinterpret_cast<bf16x8*>(&w3); }
;     else { ATT_SOFTMAX(t == 0); }
;     if constexpr (!(ABL & 4)) { ATT_WRITE_K(k2); ATT_WRITE_V(v1); }
;     ATT_SBAR();
; #pragma unroll
;     for (int ks = 0; ks < 4; ++ks) ATT_VPAIR(va, v0, 0, ks);
;     asm volatile("s_waitcnt lgkmcnt(8)" ::: "memory"); ATT_BAR();
;     ATT_XSECTION(true);
;     if constexpr (!(ABL & 4)) { const int tk = (t + 3 < NT) ? t + 3 : NT - 1, tv = (t + 2 < NT) ? t + 2 : NT - 1; ATT_LOAD_K(tk); ATT_LOAD_V(tv); }
;     ATT_BAR();
;     { const int tk_ = k0; k0 = k1; k1 = k2; k2 = tk_; const int tv_ = v0; v0 = v1; v1 = v2; v2 = tv_; }
.Lu3_join_b1_2:
	v_exp_f32_e32 v98, v98
	v_exp_f32_e32 v114, v114
	v_exp_f32_e32 v99, v99
	v_exp_f32_e32 v115, v115
	v_exp_f32_e32 v100, v100
	v_exp_f32_e32 v101, v101
	v_exp_f32_e32 v102, v102
	v_exp_f32_e32 v103, v103
	v_exp_f32_e32 v106, v106
	v_exp_f32_e32 v107, v107
	v_exp_f32_e32 v116, v116
	v_exp_f32_e32 v117, v117
	v_exp_f32_e32 v118, v118
	v_exp_f32_e32 v119, v119
	v_exp_f32_e32 v104, v104
	v_exp_f32_e32 v120, v120
	v_exp_f32_e32 v105, v105
	v_exp_f32_e32 v121, v121
	v_exp_f32_e32 v122, v122
	v_exp_f32_e32 v123, v123
	v_exp_f32_e32 v108, v108
	v_exp_f32_e32 v124, v124
	v_exp_f32_e32 v109, v109
	v_exp_f32_e32 v125, v125
	v_exp_f32_e32 v110, v110
	v_exp_f32_e32 v126, v126
	v_exp_f32_e32 v111, v111
	v_exp_f32_e32 v127, v127
	v_exp_f32_e32 v112, v112
	v_exp_f32_e32 v128, v128
	v_exp_f32_e32 v113, v113
	v_exp_f32_e32 v129, v129
	v_cvt_pk_bf16_f32 v2, v98, v99
	v_cvt_pk_bf16_f32 v3, v100, v101
	v_cvt_pk_bf16_f32 v4, v102, v103
	v_cvt_pk_bf16_f32 v6, v106, v107
	v_cvt_pk_bf16_f32 v10, v114, v115
	v_cvt_pk_bf16_f32 v5, v104, v105
	v_cvt_pk_bf16_f32 v7, v108, v109
	v_cvt_pk_bf16_f32 v8, v110, v111
	v_cvt_pk_bf16_f32 v9, v112, v113
	v_cvt_pk_bf16_f32 v11, v116, v117
	v_cvt_pk_bf16_f32 v12, v118, v119
	v_cvt_pk_bf16_f32 v13, v120, v121
	v_cvt_pk_bf16_f32 v14, v122, v123
	v_cvt_pk_bf16_f32 v15, v124, v125
	v_cvt_pk_bf16_f32 v16, v126, v127
	v_cvt_pk_bf16_f32 v17, v128, v129
	s_waitcnt vmcnt(0)
	ds_write_b128 v248, v[224:227] offset:34816
	ds_write_b128 v167, v[228:231] offset:16384
	ds_write_b128 v168, v[232:235] offset:16384
	ds_read_b128 v[152:155], v249 offset:25600
	ds_read_b128 v[156:159], v249 offset:30208
	ds_read_b128 v[160:163], v249 offset:25632
	ds_read_b128 v[176:179], v249 offset:30240
	s_waitcnt lgkmcnt(4)
	s_barrier
	s_setprio 2
	s_waitcnt lgkmcnt(3)
	v_mfma_f32_32x32x16_bf16 v[98:113], v[152:155], v[136:139], v[82:97]
	ds_read_b128 v[180:183], v249 offset:25664
	s_waitcnt lgkmcnt(3)
	v_mfma_f32_32x32x16_bf16 v[114:129], v[156:159], v[136:139], v[82:97]
	ds_read_b128 v[186:189], v249 offset:30272
	s_waitcnt lgkmcnt(3)
	v_mfma_f32_32x32x16_bf16 v[98:113], v[160:163], v[140:143], v[98:113]
	ds_read_b128 v[190:193], v249 offset:25696
	ds_read_b64_tr_b16 v[198:199], v131
	ds_read_b64_tr_b16 v[200:201], v131 offset:2048
	s_waitcnt lgkmcnt(5)
	v_mfma_f32_32x32x16_bf16 v[114:129], v[176:179], v[140:143], v[114:129]
	ds_read_b128 v[194:197], v249 offset:30304
	ds_read_b64_tr_b16 v[212:213], v131 offset:4096
	ds_read_b64_tr_b16 v[214:215], v131 offset:6144
	s_waitcnt lgkmcnt(7)
	v_mfma_f32_32x32x16_bf16 v[98:113], v[180:183], v[144:147], v[98:113]
	ds_read_b64_tr_b16 v[216:217], v131 offset:8192
	ds_read_b64_tr_b16 v[218:219], v131 offset:10240
	s_waitcnt lgkmcnt(8)
	v_mfma_f32_32x32x16_bf16 v[114:129], v[186:189], v[144:147], v[114:129]
	ds_read_b64_tr_b16 v[220:221], v131 offset:12288
	ds_read_b64_tr_b16 v[222:223], v131 offset:14336
	s_waitcnt lgkmcnt(9)
	v_mfma_f32_32x32x16_bf16 v[98:113], v[190:193], v[148:151], v[98:113]
	s_waitcnt lgkmcnt(6)
	v_mfma_f32_32x32x16_bf16 v[114:129], v[194:197], v[148:151], v[114:129]
	v_mfma_f32_32x32x16_bf16 v[18:33], v[2:5], v[198:201], v[18:33]
	ds_read_b64_tr_b16 v[236:237], v131 offset:512
	ds_read_b64_tr_b16 v[238:239], v131 offset:2560
	s_waitcnt lgkmcnt(6)
	v_mfma_f32_32x32x16_bf16 v[18:33], v[6:9], v[212:215], v[18:33]
	ds_read_b64_tr_b16 v[198:199], v131 offset:4608
	ds_read_b64_tr_b16 v[200:201], v131 offset:6656
	s_waitcnt lgkmcnt(6)
	v_mfma_f32_32x32x16_bf16 v[18:33], v[10:13], v[216:219], v[18:33]
	ds_read_b64_tr_b16 v[212:213], v131 offset:8704
	ds_read_b64_tr_b16 v[214:215], v131 offset:10752
	s_waitcnt lgkmcnt(6)
	v_mfma_f32_32x32x16_bf16 v[18:33], v[14:17], v[220:223], v[18:33]
	ds_read_b64_tr_b16 v[216:217], v131 offset:12800
	ds_read_b64_tr_b16 v[218:219], v131 offset:14848
	v_max3_f32 v152, v98, v99, v100
	s_waitcnt lgkmcnt(6)
	v_mfma_f32_32x32x16_bf16 v[34:49], v[2:5], v[236:239], v[34:49]
	ds_read_b64_tr_b16 v[220:221], v131 offset:1024
	ds_read_b64_tr_b16 v[222:223], v131 offset:3072
	v_max3_f32 v173, v114, v115, v116
	s_waitcnt lgkmcnt(6)
	v_mfma_f32_32x32x16_bf16 v[34:49], v[6:9], v[198:201], v[34:49]
	ds_read_b64_tr_b16 v[236:237], v131 offset:5120
	ds_read_b64_tr_b16 v[238:239], v131 offset:7168
	v_max3_f32 v152, v152, v101, v102
	s_waitcnt lgkmcnt(6)
	v_mfma_f32_32x32x16_bf16 v[34:49], v[10:13], v[212:215], v[34:49]
	ds_read_b64_tr_b16 v[198:199], v131 offset:9216
	ds_read_b64_tr_b16 v[200:201], v131 offset:11264
	v_max3_f32 v173, v173, v117, v118
	s_waitcnt lgkmcnt(6)
	v_mfma_f32_32x32x16_bf16 v[34:49], v[14:17], v[216:219], v[34:49]
	ds_read_b64_tr_b16 v[212:213], v131 offset:13312
	ds_read_b64_tr_b16 v[214:215], v131 offset:15360
	v_max3_f32 v152, v152, v103, v104
	s_waitcnt lgkmcnt(6)
	v_mfma_f32_32x32x16_bf16 v[50:65], v[2:5], v[220:223], v[50:65]
	ds_read_b64_tr_b16 v[216:217], v131 offset:1536
	ds_read_b64_tr_b16 v[218:219], v131 offset:3584
	v_max3_f32 v173, v173, v119, v120
	s_waitcnt lgkmcnt(6)
	v_mfma_f32_32x32x16_bf16 v[50:65], v[6:9], v[236:239], v[50:65]
	ds_read_b64_tr_b16 v[220:221], v131 offset:5632
	ds_read_b64_tr_b16 v[222:223], v131 offset:7680
	v_max3_f32 v152, v152, v105, v106
	s_waitcnt lgkmcnt(6)
	v_mfma_f32_32x32x16_bf16 v[50:65], v[10:13], v[198:201], v[50:65]
	ds_read_b64_tr_b16 v[236:237], v131 offset:9728
	ds_read_b64_tr_b16 v[238:239], v131 offset:11776
	v_max3_f32 v173, v173, v121, v122
	s_waitcnt lgkmcnt(6)
	v_mfma_f32_32x32x16_bf16 v[50:65], v[14:17], v[212:215], v[50:65]
	ds_read_b64_tr_b16 v[198:199], v131 offset:13824
	ds_read_b64_tr_b16 v[200:201], v131 offset:15872
	v_max3_f32 v152, v152, v107, v108
	s_waitcnt lgkmcnt(6)
	v_mfma_f32_32x32x16_bf16 v[66:81], v[2:5], v[216:219], v[66:81]
	v_max3_f32 v173, v173, v123, v124
	s_min_u32 s14, s97, 0x7c
	s_lshl_b32 s14, s14, 17
	s_add_i32 s14, s14, 0x60000
	buffer_load_dwordx4 v[224:227], v170, s[8:11], s14 offen
	s_waitcnt lgkmcnt(4)
	v_mfma_f32_32x32x16_bf16 v[66:81], v[6:9], v[220:223], v[66:81]
	v_max3_f32 v152, v152, v109, v110
	s_add_i32 s19, s36, 0xffff0000
	s_mov_b32 s14, s10
	s_mov_b32 s15, s11
	buffer_load_dwordx4 v[228:231], v171, s[12:15], s19 offen
	s_waitcnt lgkmcnt(2)
	v_mfma_f32_32x32x16_bf16 v[66:81], v[10:13], v[236:239], v[66:81]
	v_max3_f32 v173, v173, v125, v126
	buffer_load_dwordx4 v[232:235], v171, s[12:15], s36 offen
	s_waitcnt lgkmcnt(0)
	v_mfma_f32_32x32x16_bf16 v[66:81], v[14:17], v[198:201], v[66:81]
	v_max3_f32 v152, v152, v111, v112
	v_mfma_f32_16x16x32_bf16 v[240:243], v[2:5], v[132:135], v[240:243]
	v_max3_f32 v173, v173, v127, v128
	v_mfma_f32_16x16x32_bf16 v[240:243], v[6:9], v[132:135], v[240:243]
	v_max_f32 v152, v152, v113
	v_mfma_f32_16x16x32_bf16 v[240:243], v[10:13], v[132:135], v[240:243]
	v_max_f32 v173, v173, v129
	v_mfma_f32_16x16x32_bf16 v[240:243], v[14:17], v[132:135], v[240:243]
	v_max_f32 v173, v173, v152
	s_setprio 0
	s_barrier
	s_add_i32 s36, s36, 0x20000
	s_add_i32 s97, s97, 1
	s_cmpk_eq_i32 s97, 0x7e
	s_cbranch_scc1 .Lu3_exit_b1_2
	s_branch .Lu3_b1_0

; #define ATT_PK4(P, BASE, OUT) do { u32x4 w = {cvtpk(P[BASE + 0], P[BASE + 1]), cvtpk(P[BASE + 2], P[BASE + 3]), cvtpk(P[BASE + 4], P[BASE + 5]), cvtpk(P[BASE + 6], P[BASE + 7])}; \
;     OUT = *reinterpret_cast<bf16x8*>(&w); } while (0)
; template <int DQK> __device__ __forceinline__ void qkt(f32x16& p0, f32x16& p1, const char* Ks, const bf16x8* qr, int r32, int hi) {
;   p0 = f32x16{}; p1 = f32x16{};
; #pragma unroll
;   for (int d0 = 0; d0 < DQK / 16; ++d0) { const int cb = (d0 * 16 + hi * 8) * 2;
;     const bf16x8 b0 = *reinterpret_cast<const bf16x8*>(Ks + kswz<DQK>(r32, cb));
;     const bf16x8 b1 = *reinterpret_cast<const bf16x8*>(Ks + kswz<DQK>(32 + r32, cb));
;     p0 = __builtin_amdgcn_mfma_f32_32x32x16_bf16(b0, qr[d0], p0, 0, 0, 0);
;     p1 = __builtin_amdgcn_mfma_f32_32x32x16_bf16(b1, qr[d0], p1, 0, 0, 0); }
; }
; __device__ __forceinline__ float softmax_shift(f32x16& p0, f32x16& p1, f32x16& negm, float pmax, bool first) {
;   asm volatile("s_nop 4" ::: "memory");
;   { auto rr = __builtin_amdgcn_permlane32_swap(__float_as_uint(pmax), __float_as_uint(pmax), false, false);
;     pmax = fmaxf(__uint_as_float(rr[0]), __uint_as_float(rr[1])); }
;   const float delta = first ? pmax : fmaxf(pmax, 0.f);
; #pragma unroll
;   for (int r = 0; r < 16; ++r) { p0[r] -= delta; p1[r] -= delta; negm[r] -= delta; }
;   return first ? 1.f : __builtin_amdgcn_exp2f(-delta);
; }
; __device__ __forceinline__ void softmax_exp_pack(f32x16& p0, f32x16& p1, bf16x8& pa0, bf16x8& pa1, bf16x8& pa2, bf16x8& pa3) {
; #pragma unroll
;   for (int r = 0; r < 16; ++r) { p0[r] = __builtin_amdgcn_exp2f(p0[r]); p1[r] = __builtin_amdgcn_exp2f(p1[r]); }
;     ...
;   ATT_PK4(p0, 0, pa0); ATT_PK4(p0, 8, pa1); ATT_PK4(p1, 0, pa2); ATT_PK4(p1, 8, pa3);
.LBB0_296:
	v_mul_u32_u24_e32 v2, 0x90, v62
	v_add3_u32 v78, 0, v184, v2
	ds_read_b128 v[2:5], v78 offset:49152
	v_mad_u32_u24 v167, v62, s82, 0
	v_add_u32_e32 v173, v167, v184
	ds_read_b128 v[34:37], v173 offset:53760
	ds_read_b128 v[66:69], v78 offset:49184
	ds_read_b128 v[70:73], v78 offset:49216
	v_and_b32_e32 v63, 63, v63
	s_mov_b32 s90, 1
	s_waitcnt lgkmcnt(3)
	v_mfma_f32_32x32x16_bf16 v[2:17], v[2:5], v[136:139], 0
	s_waitcnt lgkmcnt(2)
	v_mfma_f32_32x32x16_bf16 v[34:49], v[34:37], v[136:139], 0
	s_waitcnt lgkmcnt(1)
	v_mfma_f32_32x32x16_bf16 v[2:17], v[66:69], v[140:143], v[2:17]
	ds_read_b128 v[66:69], v78 offset:53792
	ds_read_b128 v[74:77], v78 offset:49248
	s_waitcnt lgkmcnt(1)
	v_mfma_f32_32x32x16_bf16 v[34:49], v[66:69], v[140:143], v[34:49]
	v_mfma_f32_32x32x16_bf16 v[2:17], v[70:73], v[144:147], v[2:17]
	ds_read_b128 v[66:69], v78 offset:53824
	ds_read_b128 v[70:73], v78 offset:53856
	s_waitcnt lgkmcnt(1)
	v_mfma_f32_32x32x16_bf16 v[34:49], v[66:69], v[144:147], v[34:49]
	v_lshlrev_b32_e32 v67, 3, v63
	v_lshlrev_b32_e32 v69, 4, v63
	v_add_u32_e32 v66, 0xc000, v170
	v_and_b32_e32 v68, 24, v67
	v_and_b32_e32 v69, 0xc0, v69
	v_and_b32_e32 v67, 0x100, v67
	v_mfma_f32_32x32x16_bf16 v[2:17], v[74:77], v[148:151], v[2:17]
	v_lshlrev_b32_e32 v74, 1, v63
	v_and_b32_e32 v74, 32, v74
	s_waitcnt lgkmcnt(0)
	v_mfma_f32_32x32x16_bf16 v[34:49], v[70:73], v[148:151], v[34:49]
	s_barrier
	v_cmp_gt_u32_e64 s[4:5], 32, v63
	v_lshl_add_u32 v166, v62, 2, s6
	s_nop 9
	v_add_f32_e32 v62, 0, v34
	v_max3_f32 v63, v62, v2, v3
	v_max3_f32 v63, v63, v4, v5
	v_max3_f32 v63, v63, v6, v7
	v_max3_f32 v63, v63, v8, v9
	v_max3_f32 v63, v63, v10, v11
	v_max3_f32 v63, v63, v12, v13
	v_max3_f32 v63, v63, v14, v15
	v_max3_f32 v63, v63, v16, v17
	s_nop 4
	v_add3_u32 v68, 0, v68, v69
	v_max3_f32 v62, v63, v35, v36
	v_max3_f32 v62, v62, v37, v38
	v_max3_f32 v62, v62, v39, v40
	v_max3_f32 v62, v62, v41, v42
	v_max3_f32 v62, v62, v43, v44
	v_max3_f32 v62, v62, v45, v46
	v_max3_f32 v62, v62, v47, v48
	v_max_f32 v62, v62, v49
	v_add3_u32 v131, v68, v74, v67
	v_mov_b32_e32 v63, v62
	s_nop 1
	v_permlane32_swap_b32_e32 v62, v63
	v_max_f32_e32 v63, v63, v63
	v_max_f32_e32 v62, v62, v62
	v_max_f32_e32 v62, v62, v63
	v_sub_f32_e32 v2, v2, v62
	v_sub_f32_e32 v34, v34, v62
	v_sub_f32_e32 v3, v3, v62
	v_sub_f32_e32 v35, v35, v62
	v_sub_f32_e32 v4, v4, v62
	v_sub_f32_e32 v36, v36, v62
	v_sub_f32_e32 v5, v5, v62
	v_sub_f32_e32 v37, v37, v62
	v_sub_f32_e32 v6, v6, v62
	v_sub_f32_e32 v38, v38, v62
	v_sub_f32_e32 v7, v7, v62
	v_sub_f32_e32 v39, v39, v62
	v_sub_f32_e32 v8, v8, v62
	v_sub_f32_e32 v40, v40, v62
	v_sub_f32_e32 v9, v9, v62
	v_sub_f32_e32 v41, v41, v62
	v_sub_f32_e32 v10, v10, v62
	v_sub_f32_e32 v42, v42, v62
	v_sub_f32_e32 v11, v11, v62
	v_sub_f32_e32 v43, v43, v62
	v_sub_f32_e32 v12, v12, v62
	v_sub_f32_e32 v44, v44, v62
	v_sub_f32_e32 v13, v13, v62
	v_sub_f32_e32 v45, v45, v62
	v_sub_f32_e32 v14, v14, v62
	v_sub_f32_e32 v46, v46, v62
	v_sub_f32_e32 v15, v15, v62
	v_sub_f32_e32 v47, v47, v62
	v_sub_f32_e32 v16, v16, v62
	v_sub_f32_e32 v48, v48, v62
	v_sub_f32_e32 v17, v17, v62
	v_sub_f32_e32 v49, v49, v62
	v_exp_f32_e32 v2, v2
	v_exp_f32_e32 v34, v34
	v_exp_f32_e32 v3, v3
	v_exp_f32_e32 v35, v35
	v_exp_f32_e32 v4, v4
	v_exp_f32_e32 v36, v36
	v_exp_f32_e32 v5, v5
	v_exp_f32_e32 v37, v37
	v_exp_f32_e32 v6, v6
	v_exp_f32_e32 v38, v38
	v_exp_f32_e32 v7, v7
	v_exp_f32_e32 v39, v39
	v_exp_f32_e32 v8, v8
	v_exp_f32_e32 v40, v40
	v_exp_f32_e32 v9, v9
	v_exp_f32_e32 v41, v41
	v_exp_f32_e32 v10, v10
	v_exp_f32_e32 v42, v42
	v_exp_f32_e32 v11, v11
	v_exp_f32_e32 v43, v43
	v_exp_f32_e32 v12, v12
	v_exp_f32_e32 v44, v44
	v_exp_f32_e32 v13, v13
	v_exp_f32_e32 v45, v45
	v_exp_f32_e32 v14, v14
	v_exp_f32_e32 v46, v46
	v_exp_f32_e32 v15, v15
	v_exp_f32_e32 v47, v47
	v_exp_f32_e32 v16, v16
	v_exp_f32_e32 v48, v48
	v_exp_f32_e32 v17, v17
	v_exp_f32_e32 v49, v49
	v_sub_f32_e32 v82, 0, v62
	v_mov_b32_e32 v83, v82
	v_mov_b32_e32 v84, v82
	v_mov_b32_e32 v85, v82
	v_mov_b32_e32 v86, v82
	v_mov_b32_e32 v87, v82
	v_mov_b32_e32 v88, v82
	v_mov_b32_e32 v89, v82
	v_mov_b32_e32 v90, v82
	v_mov_b32_e32 v91, v82
	v_mov_b32_e32 v92, v82
	v_mov_b32_e32 v93, v82
	v_mov_b32_e32 v94, v82
	v_mov_b32_e32 v95, v82
	v_mov_b32_e32 v96, v82
	v_mov_b32_e32 v97, v82
	v_cvt_pk_bf16_f32 v98, v2, v3
	v_cvt_pk_bf16_f32 v99, v4, v5
	v_cvt_pk_bf16_f32 v100, v6, v7
	v_cvt_pk_bf16_f32 v101, v8, v9
	v_cvt_pk_bf16_f32 v102, v10, v11
	v_cvt_pk_bf16_f32 v103, v12, v13
	v_cvt_pk_bf16_f32 v104, v14, v15
	v_cvt_pk_bf16_f32 v105, v16, v17
	v_cvt_pk_bf16_f32 v106, v34, v35
	v_cvt_pk_bf16_f32 v107, v36, v37
	v_cvt_pk_bf16_f32 v108, v38, v39
	v_cvt_pk_bf16_f32 v109, v40, v41
	v_cvt_pk_bf16_f32 v110, v42, v43
	v_cvt_pk_bf16_f32 v111, v44, v45
	v_cvt_pk_bf16_f32 v112, v46, v47
	v_cvt_pk_bf16_f32 v113, v48, v49
	s_waitcnt vmcnt(1)
	ds_write_b128 v66, v[58:61] offset:18432
	ds_write_b128 v64, v[50:53] offset:16384
	s_waitcnt vmcnt(0)
	ds_write_b128 v65, v[54:57] offset:16384
	ds_read_b64_tr_b16 v[2:3], v131
	ds_read_b64_tr_b16 v[4:5], v131 offset:2048
	ds_read_b64_tr_b16 v[6:7], v131 offset:4096
	ds_read_b64_tr_b16 v[8:9], v131 offset:6144
	ds_read_b64_tr_b16 v[10:11], v131 offset:8192
	ds_read_b64_tr_b16 v[12:13], v131 offset:10240
	ds_read_b64_tr_b16 v[14:15], v131 offset:12288
	ds_read_b64_tr_b16 v[16:17], v131 offset:14336
	s_waitcnt lgkmcnt(8)
	s_barrier
; #define ATT_SBAR() __builtin_amdgcn_sched_barrier(0)
; __device__ __forceinline__ unsigned cvtpk(float lo, float hi) { f32x2_t v = {lo, hi}; bf16x2_t b = __builtin_convertvector(v, bf16x2_t); return __builtin_bit_cast(unsigned, b); }
; #define ATT_LOAD_K(t) do { const unsigned so_ = (unsigned)(t) * (unsigned)(KVBLK * LDK * 2); sk0 = __builtin_bit_cast(bf16x8, __builtin_amdgcn_raw_buffer_load_b128(krs, koff, so_, 0)); \
;     if constexpr (DQK == 128) sk1 = __builtin_bit_cast(bf16x8, __builtin_amdgcn_raw_buffer_load_b128(krs, koff, so_ + (unsigned)(32 * LDK * 2), 0)); } while (0)
; #define ATT_LOAD_V(t) do { const unsigned so_ = (unsigned)(t) * (unsigned)(KVBLK * LDV * 2); sv0 = __builtin_bit_cast(bf16x8, __builtin_amdgcn_raw_buffer_load_b128(vrs, voff, so_, 0)); \
;     sv1 = __builtin_bit_cast(bf16x8, __builtin_amdgcn_raw_buffer_load_b128(vrs, voff, so_ + (unsigned)(32 * LDV * 2), 0)); } while (0)
; #define ATT_WRITE_K(so) do { *(bf16x8*)(K_lds + (so) + kswz<DQK>(kr, kc * 2)) = sk0; if constexpr (DQK == 128) *(bf16x8*)(K_lds + (so) + kswz<DQK>(32 + kr, kc * 2)) = sk1; } while (0)
; #define ATT_WRITE_V(so) do { *(bf16x8*)(V_lds + (so) + vst0) = sv0; *(bf16x8*)(V_lds + (so) + vst1) = sv1; } while (0)
;     ...
;   for (int t = 0; t + 1 < NT; ++t) {
;     if constexpr (ABL & 1) { u32x4 w0 = {cvtpk(p0[0], p0[1]), cvtpk(p0[2], p0[3]), cvtpk(p0[4], p0[5]), cvtpk(p0[6], p0[7])}, w1 = {cvtpk(p0[8], p0[9]), cvtpk(p0[10], p0[11]), cvtpk(p0[12], p0[13]), cvtpk(p0[14], p0[15])};
;         u32x4 w2 = {cvtpk(p1[0], p1[1]), cvtpk(p1[2], p1[3]), cvtpk(p1[4], p1[5]), cvtpk(p1[6], p1[7])}, w3 = {cvtpk(p1[8], p1[9]), cvtpk(p1[10], p1[11]), cvtpk(p1[12], p1[13]), cvtpk(p1[14], p1[15])};
;         pa0 = *reinterpret_cast<bf16x8*>(&w0); pa1 = *reinterpret_cast<bf16x8*>(&w1); pa2 = *reinterpret_cast<bf16x8*>(&w2); pa3 = *reinterpret_cast<bf16x8*>(&w3); }
;     else { ATT_SOFTMAX(t == 0); }
;     if constexpr (!(ABL & 4)) { ATT_WRITE_K(k2); ATT_WRITE_V(v1); }
;     ATT_SBAR();
; #pragma unroll
;     for (int ks = 0; ks < 4; ++ks) ATT_VPAIR(va, v0, 0, ks);
;     asm volatile("s_waitcnt lgkmcnt(8)" ::: "memory"); ATT_BAR();
;     ATT_XSECTION(true);
;     if constexpr (!(ABL & 4)) { const int tk = (t + 3 < NT) ? t + 3 : NT - 1, tv = (t + 2 < NT) ? t + 2 : NT - 1; ATT_LOAD_K(tk); ATT_LOAD_V(tv); }
;     ATT_BAR();
	s_setprio 2
	s_waitcnt lgkmcnt(6)
	v_mfma_f32_32x32x16_bf16 v[66:81], v[98:101], v[2:5], 0
	ds_read_b64_tr_b16 v[34:35], v131 offset:512
	ds_read_b64_tr_b16 v[36:37], v131 offset:2560
	s_waitcnt lgkmcnt(6)
	v_mfma_f32_32x32x16_bf16 v[66:81], v[102:105], v[6:9], v[66:81]
	ds_read_b64_tr_b16 v[2:3], v131 offset:4608
	ds_read_b64_tr_b16 v[4:5], v131 offset:6656
	s_waitcnt lgkmcnt(6)
	v_mfma_f32_32x32x16_bf16 v[66:81], v[106:109], v[10:13], v[66:81]
	ds_read_b64_tr_b16 v[6:7], v131 offset:8704
	ds_read_b64_tr_b16 v[8:9], v131 offset:10752
	s_waitcnt lgkmcnt(6)
	v_mfma_f32_32x32x16_bf16 v[66:81], v[110:113], v[14:17], v[66:81]
	ds_read_b64_tr_b16 v[10:11], v131 offset:12800
	ds_read_b64_tr_b16 v[12:13], v131 offset:14848
	s_waitcnt lgkmcnt(6)
	v_mfma_f32_32x32x16_bf16 v[50:65], v[98:101], v[34:37], 0
	ds_read_b64_tr_b16 v[14:15], v131 offset:1024
	ds_read_b64_tr_b16 v[16:17], v131 offset:3072
	s_waitcnt lgkmcnt(6)
	v_mfma_f32_32x32x16_bf16 v[50:65], v[102:105], v[2:5], v[50:65]
	ds_read_b64_tr_b16 v[114:115], v131 offset:5120
	ds_read_b64_tr_b16 v[116:117], v131 offset:7168
	s_waitcnt lgkmcnt(6)
	v_mfma_f32_32x32x16_bf16 v[50:65], v[106:109], v[6:9], v[50:65]
	ds_read_b64_tr_b16 v[2:3], v131 offset:9216
	ds_read_b64_tr_b16 v[4:5], v131 offset:11264
	s_waitcnt lgkmcnt(6)
	v_mfma_f32_32x32x16_bf16 v[50:65], v[110:113], v[10:13], v[50:65]
	ds_read_b64_tr_b16 v[6:7], v131 offset:13312
	ds_read_b64_tr_b16 v[8:9], v131 offset:15360
	s_waitcnt lgkmcnt(6)
	v_mfma_f32_32x32x16_bf16 v[34:49], v[98:101], v[14:17], 0
	ds_read_b64_tr_b16 v[10:11], v131 offset:1536
	ds_read_b64_tr_b16 v[12:13], v131 offset:3584
	s_waitcnt lgkmcnt(6)
	v_mfma_f32_32x32x16_bf16 v[34:49], v[102:105], v[114:117], v[34:49]
	ds_read_b64_tr_b16 v[118:119], v131 offset:5632
	ds_read_b64_tr_b16 v[120:121], v131 offset:7680
	s_waitcnt lgkmcnt(6)
	v_mfma_f32_32x32x16_bf16 v[34:49], v[106:109], v[2:5], v[34:49]
	ds_read_b64_tr_b16 v[114:115], v131 offset:9728
	ds_read_b64_tr_b16 v[116:117], v131 offset:11776
	s_waitcnt lgkmcnt(6)
	v_mfma_f32_32x32x16_bf16 v[34:49], v[110:113], v[6:9], v[34:49]
	ds_read_b64_tr_b16 v[122:123], v131 offset:13824
	ds_read_b64_tr_b16 v[124:125], v131 offset:15872
	s_waitcnt lgkmcnt(6)
	v_mfma_f32_32x32x16_bf16 v[2:17], v[98:101], v[10:13], 0
	ds_read_b128 v[126:129], v173 offset:58368
	s_waitcnt lgkmcnt(5)
	v_mfma_f32_32x32x16_bf16 v[2:17], v[102:105], v[118:121], v[2:17]
	ds_read_b128 v[152:155], v173 offset:62976
	s_waitcnt lgkmcnt(4)
	v_mfma_f32_32x32x16_bf16 v[2:17], v[106:109], v[114:117], v[2:17]
	ds_read_b128 v[156:159], v173 offset:58400
	s_waitcnt lgkmcnt(3)
	v_mfma_f32_32x32x16_bf16 v[2:17], v[110:113], v[122:125], v[2:17]
	ds_read_b128 v[160:163], v173 offset:63008
	v_mfma_f32_16x16x32_bf16 v[240:243], v[98:101], v[132:135], 0
	ds_read_b128 v[174:177], v173 offset:58432
	v_mfma_f32_16x16x32_bf16 v[240:243], v[102:105], v[132:135], v[240:243]
	ds_read_b128 v[178:181], v173 offset:63040
	v_mfma_f32_16x16x32_bf16 v[240:243], v[106:109], v[132:135], v[240:243]
	ds_read_b128 v[186:189], v173 offset:58464
	v_mfma_f32_16x16x32_bf16 v[240:243], v[110:113], v[132:135], v[240:243]
	ds_read_b128 v[190:193], v173 offset:63072
	s_waitcnt lgkmcnt(7)
	v_mfma_f32_32x32x16_bf16 v[98:113], v[126:129], v[136:139], v[82:97]
	v_mov_b64_e32 v[128:129], v[96:97]
	v_mov_b64_e32 v[126:127], v[94:95]
	v_mov_b64_e32 v[124:125], v[92:93]
	v_mov_b64_e32 v[122:123], v[90:91]
	v_mov_b64_e32 v[120:121], v[88:89]
	v_mov_b64_e32 v[118:119], v[86:87]
	v_mov_b64_e32 v[116:117], v[84:85]
	v_mov_b64_e32 v[114:115], v[82:83]
	s_waitcnt lgkmcnt(6)
	s_nop 0
	v_mfma_f32_32x32x16_bf16 v[114:129], v[152:155], v[136:139], v[114:129]
	s_waitcnt lgkmcnt(5)
	v_mfma_f32_32x32x16_bf16 v[98:113], v[156:159], v[140:143], v[98:113]
	s_waitcnt lgkmcnt(4)
	v_mfma_f32_32x32x16_bf16 v[114:129], v[160:163], v[140:143], v[114:129]
	s_waitcnt lgkmcnt(3)
	v_mfma_f32_32x32x16_bf16 v[98:113], v[174:177], v[144:147], v[98:113]
	s_waitcnt lgkmcnt(2)
	v_mfma_f32_32x32x16_bf16 v[114:129], v[178:181], v[144:147], v[114:129]
	s_waitcnt lgkmcnt(1)
	v_mfma_f32_32x32x16_bf16 v[98:113], v[186:189], v[148:151], v[98:113]
	s_waitcnt lgkmcnt(0)
	v_mfma_f32_32x32x16_bf16 v[114:129], v[190:193], v[148:151], v[114:129]
	s_setprio 0
	buffer_load_dwordx4 v[224:227], v171, s[8:11], s85 offen
	buffer_load_dwordx4 v[228:231], v172, s[12:15], s83 offen
	buffer_load_dwordx4 v[232:235], v172, s[12:15], s86 offen
	s_barrier
	s_mov_b32 s50, 0x8000
	s_movk_i32 s15, 0x4000
	s_movk_i32 s51, 0x2400
	s_mov_b32 s49, 0
	s_movk_i32 s14, 0x4800
	s_mov_b32 s36, 0x70000
	s_mov_b32 s48, 0
	s_nop 0
	v_add_f32_e32 v174, 0, v114
	v_max3_f32 v175, v174, v98, v99
	v_max3_f32 v175, v175, v100, v101
	v_max3_f32 v175, v175, v102, v103
	v_max3_f32 v175, v175, v104, v105
	v_max3_f32 v175, v175, v106, v107
	v_max3_f32 v175, v175, v108, v109
	v_max3_f32 v175, v175, v110, v111
	v_max3_f32 v175, v175, v112, v113
	v_max3_f32 v174, v175, v115, v116
	v_max3_f32 v174, v174, v117, v118
	v_max3_f32 v174, v174, v119, v120
	v_max3_f32 v174, v174, v121, v122
	v_max3_f32 v174, v174, v123, v124
	v_max3_f32 v174, v174, v125, v126
	v_max3_f32 v174, v174, v127, v128
	v_max_f32 v174, v174, v129
	v_add_u32_e32 v248, 0x8000, v170
	v_add_u32_e32 v249, 0x8000, v173

; #define ATT_SBAR() __builtin_amdgcn_sched_barrier(0)
; __device__ __forceinline__ unsigned cvtpk(float lo, float hi) { f32x2_t v = {lo, hi}; bf16x2_t b = __builtin_convertvector(v, bf16x2_t); return __builtin_bit_cast(unsigned, b); }
; #define ATT_PK4(P, BASE, OUT) do { u32x4 w = {cvtpk(P[BASE + 0], P[BASE + 1]), cvtpk(P[BASE + 2], P[BASE + 3]), cvtpk(P[BASE + 4], P[BASE + 5]), cvtpk(P[BASE + 6], P[BASE + 7])}; \
;     OUT = *reinterpret_cast<bf16x8*>(&w); } while (0)
; #define ATT_LOAD_K(t) do { const unsigned so_ = (unsigned)(t) * (unsigned)(KVBLK * LDK * 2); sk0 = __builtin_bit_cast(bf16x8, __builtin_amdgcn_raw_buffer_load_b128(krs, koff, so_, 0)); \
;     if constexpr (DQK == 128) sk1 = __builtin_bit_cast(bf16x8, __builtin_amdgcn_raw_buffer_load_b128(krs, koff, so_ + (unsigned)(32 * LDK * 2), 0)); } while (0)
; __device__ __forceinline__ void softmax_exp_pack(f32x16& p0, f32x16& p1, bf16x8& pa0, bf16x8& pa1, bf16x8& pa2, bf16x8& pa3) {
; #pragma unroll
;   for (int r = 0; r < 16; ++r) { p0[r] = __builtin_amdgcn_exp2f(p0[r]); p1[r] = __builtin_amdgcn_exp2f(p1[r]); }
;     ...
;   ATT_PK4(p0, 0, pa0); ATT_PK4(p0, 8, pa1); ATT_PK4(p1, 0, pa2); ATT_PK4(p1, 8, pa3);
;     ...
; }
;     ...
;   for (int t = 0; t + 1 < NT; ++t) {
;     if constexpr (ABL & 1) { u32x4 w0 = {cvtpk(p0[0], p0[1]), cvtpk(p0[2], p0[3]), cvtpk(p0[4], p0[5]), cvtpk(p0[6], p0[7])}, w1 = {cvtpk(p0[8], p0[9]), cvtpk(p0[10], p0[11]), cvtpk(p0[12], p0[13]), cvtpk(p0[14], p0[15])};
;         u32x4 w2 = {cvtpk(p1[0], p1[1]), cvtpk(p1[2], p1[3]), cvtpk(p1[4], p1[5]), cvtpk(p1[6], p1[7])}, w3 = {cvtpk(p1[8], p1[9]), cvtpk(p1[10], p1[11]), cvtpk(p1[12], p1[13]), cvtpk(p1[14], p1[15])};
;         pa0 = *reinterpret_cast<bf16x8*>(&w0); pa1 = *reinterpret_cast<bf16x8*>(&w1); pa2 = *reinterpret_cast<bf16x8*>(&w2); pa3 = *reinterpret_cast<bf16x8*>(&w3); }
;     else { ATT_SOFTMAX(t == 0); }
;     if constexpr (!(ABL & 4)) { ATT_WRITE_K(k2); ATT_WRITE_V(v1); }
;     ATT_SBAR();
; #pragma unroll
;     for (int ks = 0; ks < 4; ++ks) ATT_VPAIR(va, v0, 0, ks);
;     asm volatile("s_waitcnt lgkmcnt(8)" ::: "memory"); ATT_BAR();
;     ATT_XSECTION(true);
;     if constexpr (!(ABL & 4)) { const int tk = (t + 3 < NT) ? t + 3 : NT - 1, tv = (t + 2 < NT) ? t + 2 : NT - 1; ATT_LOAD_K(tk); ATT_LOAD_V(tv); }
;     ATT_BAR();
;     { const int tk_ = k0; k0 = k1; k1 = k2; k2 = tk_; const int tv_ = v0; v0 = v1; v1 = v2; v2 = tv_; }
;   }
.LBB0_298:
	v_exp_f32_e32 v98, v98
	v_exp_f32_e32 v114, v114
	v_exp_f32_e32 v99, v99
	v_exp_f32_e32 v115, v115
	v_exp_f32_e32 v100, v100
	v_exp_f32_e32 v101, v101
	v_exp_f32_e32 v102, v102
	v_exp_f32_e32 v103, v103
	v_exp_f32_e32 v106, v106
	v_exp_f32_e32 v107, v107
	v_exp_f32_e32 v116, v116
	v_exp_f32_e32 v117, v117
	v_exp_f32_e32 v118, v118
	v_exp_f32_e32 v119, v119
	v_exp_f32_e32 v104, v104
	v_exp_f32_e32 v120, v120
	v_exp_f32_e32 v105, v105
	v_exp_f32_e32 v121, v121
	v_exp_f32_e32 v122, v122
	v_exp_f32_e32 v123, v123
	v_exp_f32_e32 v108, v108
	v_exp_f32_e32 v124, v124
	v_exp_f32_e32 v109, v109
	v_exp_f32_e32 v125, v125
	v_exp_f32_e32 v110, v110
	v_exp_f32_e32 v126, v126
	v_exp_f32_e32 v111, v111
	v_exp_f32_e32 v127, v127
	v_exp_f32_e32 v112, v112
	v_exp_f32_e32 v128, v128
	v_exp_f32_e32 v113, v113
	v_exp_f32_e32 v129, v129
	v_cvt_pk_bf16_f32 v18, v98, v99
	v_cvt_pk_bf16_f32 v19, v100, v101
	v_cvt_pk_bf16_f32 v20, v102, v103
	v_cvt_pk_bf16_f32 v22, v106, v107
	v_cvt_pk_bf16_f32 v26, v114, v115
	v_cvt_pk_bf16_f32 v21, v104, v105
	v_cvt_pk_bf16_f32 v23, v108, v109
	v_cvt_pk_bf16_f32 v24, v110, v111
	v_cvt_pk_bf16_f32 v25, v112, v113
	v_cvt_pk_bf16_f32 v27, v116, v117
	v_cvt_pk_bf16_f32 v28, v118, v119
	v_cvt_pk_bf16_f32 v29, v120, v121
	v_cvt_pk_bf16_f32 v30, v122, v123
	v_cvt_pk_bf16_f32 v31, v124, v125
	v_cvt_pk_bf16_f32 v32, v126, v127
	v_cvt_pk_bf16_f32 v33, v128, v129
	s_waitcnt vmcnt(0)
	ds_write_b128 v248, v[224:227] offset:16384
	ds_write_b128 v168, v[228:231] offset:32768
	ds_write_b128 v169, v[232:235] offset:32768
	ds_read_b128 v[152:155], v249 offset:34816
	ds_read_b128 v[156:159], v249 offset:39424
	ds_read_b128 v[160:163], v249 offset:34848
	ds_read_b128 v[176:179], v249 offset:39456
	s_waitcnt lgkmcnt(4)
	s_barrier
	s_setprio 2
	s_waitcnt lgkmcnt(3)
	v_mfma_f32_32x32x16_bf16 v[98:113], v[152:155], v[136:139], v[82:97]
	ds_read_b128 v[180:183], v249 offset:34880
	s_waitcnt lgkmcnt(3)
	v_mfma_f32_32x32x16_bf16 v[114:129], v[156:159], v[136:139], v[82:97]
	ds_read_b128 v[186:189], v249 offset:39488
	s_waitcnt lgkmcnt(3)
	v_mfma_f32_32x32x16_bf16 v[98:113], v[160:163], v[140:143], v[98:113]
	ds_read_b128 v[190:193], v249 offset:34912
	ds_read_b64_tr_b16 v[198:199], v131 offset:16384
	ds_read_b64_tr_b16 v[200:201], v131 offset:18432
	s_waitcnt lgkmcnt(5)
	v_mfma_f32_32x32x16_bf16 v[114:129], v[176:179], v[140:143], v[114:129]
	ds_read_b128 v[194:197], v249 offset:39520
	ds_read_b64_tr_b16 v[212:213], v131 offset:20480
	ds_read_b64_tr_b16 v[214:215], v131 offset:22528
	s_waitcnt lgkmcnt(7)
	v_mfma_f32_32x32x16_bf16 v[98:113], v[180:183], v[144:147], v[98:113]
	ds_read_b64_tr_b16 v[216:217], v131 offset:24576
	ds_read_b64_tr_b16 v[218:219], v131 offset:26624
	s_waitcnt lgkmcnt(8)
	v_mfma_f32_32x32x16_bf16 v[114:129], v[186:189], v[144:147], v[114:129]
	ds_read_b64_tr_b16 v[220:221], v131 offset:28672
	ds_read_b64_tr_b16 v[222:223], v131 offset:30720
	s_waitcnt lgkmcnt(9)
	v_mfma_f32_32x32x16_bf16 v[98:113], v[190:193], v[148:151], v[98:113]
	s_waitcnt lgkmcnt(6)
	v_mfma_f32_32x32x16_bf16 v[114:129], v[194:197], v[148:151], v[114:129]
	v_mfma_f32_32x32x16_bf16 v[66:81], v[18:21], v[198:201], v[66:81]
	ds_read_b64_tr_b16 v[236:237], v131 offset:16896
	ds_read_b64_tr_b16 v[238:239], v131 offset:18944
	s_waitcnt lgkmcnt(6)
	v_mfma_f32_32x32x16_bf16 v[66:81], v[22:25], v[212:215], v[66:81]
	ds_read_b64_tr_b16 v[198:199], v131 offset:20992
	ds_read_b64_tr_b16 v[200:201], v131 offset:23040
	s_waitcnt lgkmcnt(6)
	v_mfma_f32_32x32x16_bf16 v[66:81], v[26:29], v[216:219], v[66:81]
	ds_read_b64_tr_b16 v[212:213], v131 offset:25088
	ds_read_b64_tr_b16 v[214:215], v131 offset:27136
	s_waitcnt lgkmcnt(6)
	v_mfma_f32_32x32x16_bf16 v[66:81], v[30:33], v[220:223], v[66:81]
	ds_read_b64_tr_b16 v[216:217], v131 offset:29184
	ds_read_b64_tr_b16 v[218:219], v131 offset:31232
	v_max3_f32 v152, v98, v99, v100
	s_waitcnt lgkmcnt(6)
	v_mfma_f32_32x32x16_bf16 v[50:65], v[18:21], v[236:239], v[50:65]
	ds_read_b64_tr_b16 v[220:221], v131 offset:17408
	ds_read_b64_tr_b16 v[222:223], v131 offset:19456
	v_max3_f32 v174, v114, v115, v116
	s_waitcnt lgkmcnt(6)
	v_mfma_f32_32x32x16_bf16 v[50:65], v[22:25], v[198:201], v[50:65]
	ds_read_b64_tr_b16 v[236:237], v131 offset:21504
	ds_read_b64_tr_b16 v[238:239], v131 offset:23552
	v_max3_f32 v152, v152, v101, v102
	s_waitcnt lgkmcnt(6)
	v_mfma_f32_32x32x16_bf16 v[50:65], v[26:29], v[212:215], v[50:65]
	ds_read_b64_tr_b16 v[198:199], v131 offset:25600
	ds_read_b64_tr_b16 v[200:201], v131 offset:27648
	v_max3_f32 v174, v174, v117, v118
	s_waitcnt lgkmcnt(6)
	v_mfma_f32_32x32x16_bf16 v[50:65], v[30:33], v[216:219], v[50:65]
	ds_read_b64_tr_b16 v[212:213], v131 offset:29696
	ds_read_b64_tr_b16 v[214:215], v131 offset:31744
	v_max3_f32 v152, v152, v103, v104
	s_waitcnt lgkmcnt(6)
	v_mfma_f32_32x32x16_bf16 v[34:49], v[18:21], v[220:223], v[34:49]
	ds_read_b64_tr_b16 v[216:217], v131 offset:17920
	ds_read_b64_tr_b16 v[218:219], v131 offset:19968
	v_max3_f32 v174, v174, v119, v120
	s_waitcnt lgkmcnt(6)
	v_mfma_f32_32x32x16_bf16 v[34:49], v[22:25], v[236:239], v[34:49]
	ds_read_b64_tr_b16 v[220:221], v131 offset:22016
	ds_read_b64_tr_b16 v[222:223], v131 offset:24064
	v_max3_f32 v152, v152, v105, v106
	s_waitcnt lgkmcnt(6)
	v_mfma_f32_32x32x16_bf16 v[34:49], v[26:29], v[198:201], v[34:49]
	ds_read_b64_tr_b16 v[236:237], v131 offset:26112
	ds_read_b64_tr_b16 v[238:239], v131 offset:28160
	v_max3_f32 v174, v174, v121, v122
	s_waitcnt lgkmcnt(6)
	v_mfma_f32_32x32x16_bf16 v[34:49], v[30:33], v[212:215], v[34:49]
	ds_read_b64_tr_b16 v[198:199], v131 offset:30208
	ds_read_b64_tr_b16 v[200:201], v131 offset:32256
	v_max3_f32 v152, v152, v107, v108
	s_waitcnt lgkmcnt(6)
	v_mfma_f32_32x32x16_bf16 v[2:17], v[18:21], v[216:219], v[2:17]
	v_max3_f32 v174, v174, v123, v124
	s_min_u32 s14, s90, 0x7c
	s_lshl_b32 s14, s14, 17
	s_add_i32 s19, s14, 0x60000
	s_add_i32 s92, s36, 0xffff0000
	s_mov_b32 s14, s10
	s_mov_b32 s15, s11
	buffer_load_dwordx4 v[224:227], v171, s[8:11], s19 offen
	s_waitcnt lgkmcnt(4)
	v_mfma_f32_32x32x16_bf16 v[2:17], v[22:25], v[220:223], v[2:17]
	v_max3_f32 v152, v152, v109, v110
	buffer_load_dwordx4 v[228:231], v172, s[12:15], s92 offen
	s_waitcnt lgkmcnt(2)
	v_mfma_f32_32x32x16_bf16 v[2:17], v[26:29], v[236:239], v[2:17]
	v_max3_f32 v174, v174, v125, v126
	buffer_load_dwordx4 v[232:235], v172, s[12:15], s36 offen
	s_waitcnt lgkmcnt(0)
	v_mfma_f32_32x32x16_bf16 v[2:17], v[30:33], v[198:201], v[2:17]
	v_max3_f32 v152, v152, v111, v112
	v_mfma_f32_16x16x32_bf16 v[240:243], v[18:21], v[132:135], v[240:243]
	v_max3_f32 v174, v174, v127, v128
	v_mfma_f32_16x16x32_bf16 v[240:243], v[22:25], v[132:135], v[240:243]
	v_max_f32 v152, v152, v113
	v_mfma_f32_16x16x32_bf16 v[240:243], v[26:29], v[132:135], v[240:243]
	v_max_f32 v174, v174, v129
	v_mfma_f32_16x16x32_bf16 v[240:243], v[30:33], v[132:135], v[240:243]
	v_max_f32 v174, v174, v152
	s_setprio 0
	s_barrier
	s_add_i32 s36, s36, 0x20000
	s_add_i32 s90, s90, 1
	s_cmpk_eq_i32 s90, 0x7e
	s_cbranch_scc1 .Lu3_exit_b2_0

; #define ATT_SBAR() __builtin_amdgcn_sched_barrier(0)
; __device__ __forceinline__ unsigned cvtpk(float lo, float hi) { f32x2_t v = {lo, hi}; bf16x2_t b = __builtin_convertvector(v, bf16x2_t); return __builtin_bit_cast(unsigned, b); }
; #define ATT_PK4(P, BASE, OUT) do { u32x4 w = {cvtpk(P[BASE + 0], P[BASE + 1]), cvtpk(P[BASE + 2], P[BASE + 3]), cvtpk(P[BASE + 4], P[BASE + 5]), cvtpk(P[BASE + 6], P[BASE + 7])}; \
;     OUT = *reinterpret_cast<bf16x8*>(&w); } while (0)
; #define ATT_LOAD_K(t) do { const unsigned so_ = (unsigned)(t) * (unsigned)(KVBLK * LDK * 2); sk0 = __builtin_bit_cast(bf16x8, __builtin_amdgcn_raw_buffer_load_b128(krs, koff, so_, 0)); \
;     if constexpr (DQK == 128) sk1 = __builtin_bit_cast(bf16x8, __builtin_amdgcn_raw_buffer_load_b128(krs, koff, so_ + (unsigned)(32 * LDK * 2), 0)); } while (0)
; __device__ __forceinline__ void softmax_exp_pack(f32x16& p0, f32x16& p1, bf16x8& pa0, bf16x8& pa1, bf16x8& pa2, bf16x8& pa3) {
; #pragma unroll
;   for (int r = 0; r < 16; ++r) { p0[r] = __builtin_amdgcn_exp2f(p0[r]); p1[r] = __builtin_amdgcn_exp2f(p1[r]); }
;     ...
;   ATT_PK4(p0, 0, pa0); ATT_PK4(p0, 8, pa1); ATT_PK4(p1, 0, pa2); ATT_PK4(p1, 8, pa3);
;     ...
; }
;     ...
;   for (int t = 0; t + 1 < NT; ++t) {
;     if constexpr (ABL & 1) { u32x4 w0 = {cvtpk(p0[0], p0[1]), cvtpk(p0[2], p0[3]), cvtpk(p0[4], p0[5]), cvtpk(p0[6], p0[7])}, w1 = {cvtpk(p0[8], p0[9]), cvtpk(p0[10], p0[11]), cvtpk(p0[12], p0[13]), cvtpk(p0[14], p0[15])};
;         u32x4 w2 = {cvtpk(p1[0], p1[1]), cvtpk(p1[2], p1[3]), cvtpk(p1[4], p1[5]), cvtpk(p1[6], p1[7])}, w3 = {cvtpk(p1[8], p1[9]), cvtpk(p1[10], p1[11]), cvtpk(p1[12], p1[13]), cvtpk(p1[14], p1[15])};
;         pa0 = *reinterpret_cast<bf16x8*>(&w0); pa1 = *reinterpret_cast<bf16x8*>(&w1); pa2 = *reinterpret_cast<bf16x8*>(&w2); pa3 = *reinterpret_cast<bf16x8*>(&w3); }
;     else { ATT_SOFTMAX(t == 0); }
;     if constexpr (!(ABL & 4)) { ATT_WRITE_K(k2); ATT_WRITE_V(v1); }
;     ATT_SBAR();
; #pragma unroll
;     for (int ks = 0; ks < 4; ++ks) ATT_VPAIR(va, v0, 0, ks);
;     asm volatile("s_waitcnt lgkmcnt(8)" ::: "memory"); ATT_BAR();
;     ATT_XSECTION(true);
;     if constexpr (!(ABL & 4)) { const int tk = (t + 3 < NT) ? t + 3 : NT - 1, tv = (t + 2 < NT) ? t + 2 : NT - 1; ATT_LOAD_K(tk); ATT_LOAD_V(tv); }
;     ATT_BAR();
;     { const int tk_ = k0; k0 = k1; k1 = k2; k2 = tk_; const int tv_ = v0; v0 = v1; v1 = v2; v2 = tv_; }
;   }
.Lu3_join_b2_1:
	v_exp_f32_e32 v98, v98
	v_exp_f32_e32 v114, v114
	v_exp_f32_e32 v99, v99
	v_exp_f32_e32 v115, v115
	v_exp_f32_e32 v100, v100
	v_exp_f32_e32 v101, v101
	v_exp_f32_e32 v102, v102
	v_exp_f32_e32 v103, v103
	v_exp_f32_e32 v106, v106
	v_exp_f32_e32 v107, v107
	v_exp_f32_e32 v116, v116
	v_exp_f32_e32 v117, v117
	v_exp_f32_e32 v118, v118
	v_exp_f32_e32 v119, v119
	v_exp_f32_e32 v104, v104
	v_exp_f32_e32 v120, v120
	v_exp_f32_e32 v105, v105
	v_exp_f32_e32 v121, v121
	v_exp_f32_e32 v122, v122
	v_exp_f32_e32 v123, v123
	v_exp_f32_e32 v108, v108
	v_exp_f32_e32 v124, v124
	v_exp_f32_e32 v109, v109
	v_exp_f32_e32 v125, v125
	v_exp_f32_e32 v110, v110
	v_exp_f32_e32 v126, v126
	v_exp_f32_e32 v111, v111
	v_exp_f32_e32 v127, v127
	v_exp_f32_e32 v112, v112
	v_exp_f32_e32 v128, v128
	v_exp_f32_e32 v113, v113
	v_exp_f32_e32 v129, v129
	v_cvt_pk_bf16_f32 v18, v98, v99
	v_cvt_pk_bf16_f32 v19, v100, v101
	v_cvt_pk_bf16_f32 v20, v102, v103
	v_cvt_pk_bf16_f32 v22, v106, v107
	v_cvt_pk_bf16_f32 v26, v114, v115
	v_cvt_pk_bf16_f32 v21, v104, v105
	v_cvt_pk_bf16_f32 v23, v108, v109
	v_cvt_pk_bf16_f32 v24, v110, v111
	v_cvt_pk_bf16_f32 v25, v112, v113
	v_cvt_pk_bf16_f32 v27, v116, v117
	v_cvt_pk_bf16_f32 v28, v118, v119
	v_cvt_pk_bf16_f32 v29, v120, v121
	v_cvt_pk_bf16_f32 v30, v122, v123
	v_cvt_pk_bf16_f32 v31, v124, v125
	v_cvt_pk_bf16_f32 v32, v126, v127
	v_cvt_pk_bf16_f32 v33, v128, v129
	s_waitcnt vmcnt(0)
	ds_write_b128 v248, v[224:227] offset:25600
	ds_write_b128 v168, v[228:231]
	ds_write_b128 v169, v[232:235]
	ds_read_b128 v[152:155], v249 offset:16384
	ds_read_b128 v[156:159], v249 offset:20992
	ds_read_b128 v[160:163], v249 offset:16416
	ds_read_b128 v[176:179], v249 offset:21024
	s_waitcnt lgkmcnt(4)
	s_barrier
	s_setprio 2
	s_waitcnt lgkmcnt(3)
	v_mfma_f32_32x32x16_bf16 v[98:113], v[152:155], v[136:139], v[82:97]
	ds_read_b128 v[180:183], v249 offset:16448
	s_waitcnt lgkmcnt(3)
	v_mfma_f32_32x32x16_bf16 v[114:129], v[156:159], v[136:139], v[82:97]
	ds_read_b128 v[186:189], v249 offset:21056
	s_waitcnt lgkmcnt(3)
	v_mfma_f32_32x32x16_bf16 v[98:113], v[160:163], v[140:143], v[98:113]
	ds_read_b128 v[190:193], v249 offset:16480
	ds_read_b64_tr_b16 v[198:199], v131 offset:32768
	ds_read_b64_tr_b16 v[200:201], v131 offset:34816
	s_waitcnt lgkmcnt(5)
	v_mfma_f32_32x32x16_bf16 v[114:129], v[176:179], v[140:143], v[114:129]
	ds_read_b128 v[194:197], v249 offset:21088
	ds_read_b64_tr_b16 v[212:213], v131 offset:36864
	ds_read_b64_tr_b16 v[214:215], v131 offset:38912
	s_waitcnt lgkmcnt(7)
	v_mfma_f32_32x32x16_bf16 v[98:113], v[180:183], v[144:147], v[98:113]
	ds_read_b64_tr_b16 v[216:217], v131 offset:40960
	ds_read_b64_tr_b16 v[218:219], v131 offset:43008
	s_waitcnt lgkmcnt(8)
	v_mfma_f32_32x32x16_bf16 v[114:129], v[186:189], v[144:147], v[114:129]
	ds_read_b64_tr_b16 v[220:221], v131 offset:45056
	ds_read_b64_tr_b16 v[222:223], v131 offset:47104
	s_waitcnt lgkmcnt(9)
	v_mfma_f32_32x32x16_bf16 v[98:113], v[190:193], v[148:151], v[98:113]
	s_waitcnt lgkmcnt(6)
	v_mfma_f32_32x32x16_bf16 v[114:129], v[194:197], v[148:151], v[114:129]
	v_mfma_f32_32x32x16_bf16 v[66:81], v[18:21], v[198:201], v[66:81]
	ds_read_b64_tr_b16 v[236:237], v131 offset:33280
	ds_read_b64_tr_b16 v[238:239], v131 offset:35328
	s_waitcnt lgkmcnt(6)
	v_mfma_f32_32x32x16_bf16 v[66:81], v[22:25], v[212:215], v[66:81]
	ds_read_b64_tr_b16 v[198:199], v131 offset:37376
	ds_read_b64_tr_b16 v[200:201], v131 offset:39424
	s_waitcnt lgkmcnt(6)
	v_mfma_f32_32x32x16_bf16 v[66:81], v[26:29], v[216:219], v[66:81]
	ds_read_b64_tr_b16 v[212:213], v131 offset:41472
	ds_read_b64_tr_b16 v[214:215], v131 offset:43520
	s_waitcnt lgkmcnt(6)
	v_mfma_f32_32x32x16_bf16 v[66:81], v[30:33], v[220:223], v[66:81]
	ds_read_b64_tr_b16 v[216:217], v131 offset:45568
	ds_read_b64_tr_b16 v[218:219], v131 offset:47616
	v_max3_f32 v152, v98, v99, v100
	s_waitcnt lgkmcnt(6)
	v_mfma_f32_32x32x16_bf16 v[50:65], v[18:21], v[236:239], v[50:65]
	ds_read_b64_tr_b16 v[220:221], v131 offset:33792
	ds_read_b64_tr_b16 v[222:223], v131 offset:35840
	v_max3_f32 v174, v114, v115, v116
	s_waitcnt lgkmcnt(6)
	v_mfma_f32_32x32x16_bf16 v[50:65], v[22:25], v[198:201], v[50:65]
	ds_read_b64_tr_b16 v[236:237], v131 offset:37888
	ds_read_b64_tr_b16 v[238:239], v131 offset:39936
	v_max3_f32 v152, v152, v101, v102
	s_waitcnt lgkmcnt(6)
	v_mfma_f32_32x32x16_bf16 v[50:65], v[26:29], v[212:215], v[50:65]
	ds_read_b64_tr_b16 v[198:199], v131 offset:41984
	ds_read_b64_tr_b16 v[200:201], v131 offset:44032
	v_max3_f32 v174, v174, v117, v118
	s_waitcnt lgkmcnt(6)
	v_mfma_f32_32x32x16_bf16 v[50:65], v[30:33], v[216:219], v[50:65]
	ds_read_b64_tr_b16 v[212:213], v131 offset:46080
	ds_read_b64_tr_b16 v[214:215], v131 offset:48128
	v_max3_f32 v152, v152, v103, v104
	s_waitcnt lgkmcnt(6)
	v_mfma_f32_32x32x16_bf16 v[34:49], v[18:21], v[220:223], v[34:49]
	ds_read_b64_tr_b16 v[216:217], v131 offset:34304
	ds_read_b64_tr_b16 v[218:219], v131 offset:36352
	v_max3_f32 v174, v174, v119, v120
	s_waitcnt lgkmcnt(6)
	v_mfma_f32_32x32x16_bf16 v[34:49], v[22:25], v[236:239], v[34:49]
	ds_read_b64_tr_b16 v[220:221], v131 offset:38400
	ds_read_b64_tr_b16 v[222:223], v131 offset:40448
	v_max3_f32 v152, v152, v105, v106
	s_waitcnt lgkmcnt(6)
	v_mfma_f32_32x32x16_bf16 v[34:49], v[26:29], v[198:201], v[34:49]
	ds_read_b64_tr_b16 v[236:237], v131 offset:42496
	ds_read_b64_tr_b16 v[238:239], v131 offset:44544
	v_max3_f32 v174, v174, v121, v122
	s_waitcnt lgkmcnt(6)
	v_mfma_f32_32x32x16_bf16 v[34:49], v[30:33], v[212:215], v[34:49]
	ds_read_b64_tr_b16 v[198:199], v131 offset:46592
	ds_read_b64_tr_b16 v[200:201], v131 offset:48640
	v_max3_f32 v152, v152, v107, v108
	s_waitcnt lgkmcnt(6)
	v_mfma_f32_32x32x16_bf16 v[2:17], v[18:21], v[216:219], v[2:17]
	v_max3_f32 v174, v174, v123, v124
	s_min_u32 s14, s90, 0x7c
	s_lshl_b32 s14, s14, 17
	s_add_i32 s19, s14, 0x60000
	s_add_i32 s92, s36, 0xffff0000
	s_mov_b32 s14, s10
	s_mov_b32 s15, s11
	buffer_load_dwordx4 v[224:227], v171, s[8:11], s19 offen
	s_waitcnt lgkmcnt(4)
	v_mfma_f32_32x32x16_bf16 v[2:17], v[22:25], v[220:223], v[2:17]
	v_max3_f32 v152, v152, v109, v110
	buffer_load_dwordx4 v[228:231], v172, s[12:15], s92 offen
	s_waitcnt lgkmcnt(2)
	v_mfma_f32_32x32x16_bf16 v[2:17], v[26:29], v[236:239], v[2:17]
	v_max3_f32 v174, v174, v125, v126
	buffer_load_dwordx4 v[232:235], v172, s[12:15], s36 offen
	s_waitcnt lgkmcnt(0)
	v_mfma_f32_32x32x16_bf16 v[2:17], v[30:33], v[198:201], v[2:17]
	v_max3_f32 v152, v152, v111, v112
	v_mfma_f32_16x16x32_bf16 v[240:243], v[18:21], v[132:135], v[240:243]
	v_max3_f32 v174, v174, v127, v128
	v_mfma_f32_16x16x32_bf16 v[240:243], v[22:25], v[132:135], v[240:243]
	v_max_f32 v152, v152, v113
	v_mfma_f32_16x16x32_bf16 v[240:243], v[26:29], v[132:135], v[240:243]
	v_max_f32 v174, v174, v129
	v_mfma_f32_16x16x32_bf16 v[240:243], v[30:33], v[132:135], v[240:243]
	v_max_f32 v174, v174, v152
	s_setprio 0
	s_barrier
	s_add_i32 s36, s36, 0x20000
	s_add_i32 s90, s90, 1
	s_cmpk_eq_i32 s90, 0x7e
	s_cbranch_scc1 .Lu3_exit_b2_1

; #define ATT_SBAR() __builtin_amdgcn_sched_barrier(0)
; __device__ __forceinline__ unsigned cvtpk(float lo, float hi) { f32x2_t v = {lo, hi}; bf16x2_t b = __builtin_convertvector(v, bf16x2_t); return __builtin_bit_cast(unsigned, b); }
; #define ATT_PK4(P, BASE, OUT) do { u32x4 w = {cvtpk(P[BASE + 0], P[BASE + 1]), cvtpk(P[BASE + 2], P[BASE + 3]), cvtpk(P[BASE + 4], P[BASE + 5]), cvtpk(P[BASE + 6], P[BASE + 7])}; \
;     OUT = *reinterpret_cast<bf16x8*>(&w); } while (0)
; #define ATT_LOAD_K(t) do { const unsigned so_ = (unsigned)(t) * (unsigned)(KVBLK * LDK * 2); sk0 = __builtin_bit_cast(bf16x8, __builtin_amdgcn_raw_buffer_load_b128(krs, koff, so_, 0)); \
;     if constexpr (DQK == 128) sk1 = __builtin_bit_cast(bf16x8, __builtin_amdgcn_raw_buffer_load_b128(krs, koff, so_ + (unsigned)(32 * LDK * 2), 0)); } while (0)
; __device__ __forceinline__ void softmax_exp_pack(f32x16& p0, f32x16& p1, bf16x8& pa0, bf16x8& pa1, bf16x8& pa2, bf16x8& pa3) {
; #pragma unroll
;   for (int r = 0; r < 16; ++r) { p0[r] = __builtin_amdgcn_exp2f(p0[r]); p1[r] = __builtin_amdgcn_exp2f(p1[r]); }
;     ...
;   ATT_PK4(p0, 0, pa0); ATT_PK4(p0, 8, pa1); ATT_PK4(p1, 0, pa2); ATT_PK4(p1, 8, pa3);
;     ...
; }
;     ...
;   for (int t = 0; t + 1 < NT; ++t) {
;     if constexpr (ABL & 1) { u32x4 w0 = {cvtpk(p0[0], p0[1]), cvtpk(p0[2], p0[3]), cvtpk(p0[4], p0[5]), cvtpk(p0[6], p0[7])}, w1 = {cvtpk(p0[8], p0[9]), cvtpk(p0[10], p0[11]), cvtpk(p0[12], p0[13]), cvtpk(p0[14], p0[15])};
;         u32x4 w2 = {cvtpk(p1[0], p1[1]), cvtpk(p1[2], p1[3]), cvtpk(p1[4], p1[5]), cvtpk(p1[6], p1[7])}, w3 = {cvtpk(p1[8], p1[9]), cvtpk(p1[10], p1[11]), cvtpk(p1[12], p1[13]), cvtpk(p1[14], p1[15])};
;         pa0 = *reinterpret_cast<bf16x8*>(&w0); pa1 = *reinterpret_cast<bf16x8*>(&w1); pa2 = *reinterpret_cast<bf16x8*>(&w2); pa3 = *reinterpret_cast<bf16x8*>(&w3); }
;     else { ATT_SOFTMAX(t == 0); }
;     if constexpr (!(ABL & 4)) { ATT_WRITE_K(k2); ATT_WRITE_V(v1); }
;     ATT_SBAR();
; #pragma unroll
;     for (int ks = 0; ks < 4; ++ks) ATT_VPAIR(va, v0, 0, ks);
;     asm volatile("s_waitcnt lgkmcnt(8)" ::: "memory"); ATT_BAR();
;     ATT_XSECTION(true);
;     if constexpr (!(ABL & 4)) { const int tk = (t + 3 < NT) ? t + 3 : NT - 1, tv = (t + 2 < NT) ? t + 2 : NT - 1; ATT_LOAD_K(tk); ATT_LOAD_V(tv); }
;     ATT_BAR();
;     { const int tk_ = k0; k0 = k1; k1 = k2; k2 = tk_; const int tv_ = v0; v0 = v1; v1 = v2; v2 = tv_; }
;   }
.Lu3_join_b2_2:
	v_exp_f32_e32 v98, v98
	v_exp_f32_e32 v114, v114
	v_exp_f32_e32 v99, v99
	v_exp_f32_e32 v115, v115
	v_exp_f32_e32 v100, v100
	v_exp_f32_e32 v101, v101
	v_exp_f32_e32 v102, v102
	v_exp_f32_e32 v103, v103
	v_exp_f32_e32 v106, v106
	v_exp_f32_e32 v107, v107
	v_exp_f32_e32 v116, v116
	v_exp_f32_e32 v117, v117
	v_exp_f32_e32 v118, v118
	v_exp_f32_e32 v119, v119
	v_exp_f32_e32 v104, v104
	v_exp_f32_e32 v120, v120
	v_exp_f32_e32 v105, v105
	v_exp_f32_e32 v121, v121
	v_exp_f32_e32 v122, v122
	v_exp_f32_e32 v123, v123
	v_exp_f32_e32 v108, v108
	v_exp_f32_e32 v124, v124
	v_exp_f32_e32 v109, v109
	v_exp_f32_e32 v125, v125
	v_exp_f32_e32 v110, v110
	v_exp_f32_e32 v126, v126
	v_exp_f32_e32 v111, v111
	v_exp_f32_e32 v127, v127
	v_exp_f32_e32 v112, v112
	v_exp_f32_e32 v128, v128
	v_exp_f32_e32 v113, v113
	v_exp_f32_e32 v129, v129
	v_cvt_pk_bf16_f32 v18, v98, v99
	v_cvt_pk_bf16_f32 v19, v100, v101
	v_cvt_pk_bf16_f32 v20, v102, v103
	v_cvt_pk_bf16_f32 v22, v106, v107
	v_cvt_pk_bf16_f32 v26, v114, v115
	v_cvt_pk_bf16_f32 v21, v104, v105
	v_cvt_pk_bf16_f32 v23, v108, v109
	v_cvt_pk_bf16_f32 v24, v110, v111
	v_cvt_pk_bf16_f32 v25, v112, v113
	v_cvt_pk_bf16_f32 v27, v116, v117
	v_cvt_pk_bf16_f32 v28, v118, v119
	v_cvt_pk_bf16_f32 v29, v120, v121
	v_cvt_pk_bf16_f32 v30, v122, v123
	v_cvt_pk_bf16_f32 v31, v124, v125
	v_cvt_pk_bf16_f32 v32, v126, v127
	v_cvt_pk_bf16_f32 v33, v128, v129
	s_waitcnt vmcnt(0)
	ds_write_b128 v248, v[224:227] offset:34816
	ds_write_b128 v168, v[228:231] offset:16384
	ds_write_b128 v169, v[232:235] offset:16384
	ds_read_b128 v[152:155], v249 offset:25600
	ds_read_b128 v[156:159], v249 offset:30208
	ds_read_b128 v[160:163], v249 offset:25632
	ds_read_b128 v[176:179], v249 offset:30240
	s_waitcnt lgkmcnt(4)
	s_barrier
	s_setprio 2
	s_waitcnt lgkmcnt(3)
	v_mfma_f32_32x32x16_bf16 v[98:113], v[152:155], v[136:139], v[82:97]
	ds_read_b128 v[180:183], v249 offset:25664
	s_waitcnt lgkmcnt(3)
	v_mfma_f32_32x32x16_bf16 v[114:129], v[156:159], v[136:139], v[82:97]
	ds_read_b128 v[186:189], v249 offset:30272
	s_waitcnt lgkmcnt(3)
	v_mfma_f32_32x32x16_bf16 v[98:113], v[160:163], v[140:143], v[98:113]
	ds_read_b128 v[190:193], v249 offset:25696
	ds_read_b64_tr_b16 v[198:199], v131
	ds_read_b64_tr_b16 v[200:201], v131 offset:2048
	s_waitcnt lgkmcnt(5)
	v_mfma_f32_32x32x16_bf16 v[114:129], v[176:179], v[140:143], v[114:129]
	ds_read_b128 v[194:197], v249 offset:30304
	ds_read_b64_tr_b16 v[212:213], v131 offset:4096
	ds_read_b64_tr_b16 v[214:215], v131 offset:6144
	s_waitcnt lgkmcnt(7)
	v_mfma_f32_32x32x16_bf16 v[98:113], v[180:183], v[144:147], v[98:113]
	ds_read_b64_tr_b16 v[216:217], v131 offset:8192
	ds_read_b64_tr_b16 v[218:219], v131 offset:10240
	s_waitcnt lgkmcnt(8)
	v_mfma_f32_32x32x16_bf16 v[114:129], v[186:189], v[144:147], v[114:129]
	ds_read_b64_tr_b16 v[220:221], v131 offset:12288
	ds_read_b64_tr_b16 v[222:223], v131 offset:14336
	s_waitcnt lgkmcnt(9)
	v_mfma_f32_32x32x16_bf16 v[98:113], v[190:193], v[148:151], v[98:113]
	s_waitcnt lgkmcnt(6)
	v_mfma_f32_32x32x16_bf16 v[114:129], v[194:197], v[148:151], v[114:129]
	v_mfma_f32_32x32x16_bf16 v[66:81], v[18:21], v[198:201], v[66:81]
	ds_read_b64_tr_b16 v[236:237], v131 offset:512
	ds_read_b64_tr_b16 v[238:239], v131 offset:2560
	s_waitcnt lgkmcnt(6)
	v_mfma_f32_32x32x16_bf16 v[66:81], v[22:25], v[212:215], v[66:81]
	ds_read_b64_tr_b16 v[198:199], v131 offset:4608
	ds_read_b64_tr_b16 v[200:201], v131 offset:6656
	s_waitcnt lgkmcnt(6)
	v_mfma_f32_32x32x16_bf16 v[66:81], v[26:29], v[216:219], v[66:81]
	ds_read_b64_tr_b16 v[212:213], v131 offset:8704
	ds_read_b64_tr_b16 v[214:215], v131 offset:10752
	s_waitcnt lgkmcnt(6)
	v_mfma_f32_32x32x16_bf16 v[66:81], v[30:33], v[220:223], v[66:81]
	ds_read_b64_tr_b16 v[216:217], v131 offset:12800
	ds_read_b64_tr_b16 v[218:219], v131 offset:14848
	v_max3_f32 v152, v98, v99, v100
	s_waitcnt lgkmcnt(6)
	v_mfma_f32_32x32x16_bf16 v[50:65], v[18:21], v[236:239], v[50:65]
	ds_read_b64_tr_b16 v[220:221], v131 offset:1024
	ds_read_b64_tr_b16 v[222:223], v131 offset:3072
	v_max3_f32 v174, v114, v115, v116
	s_waitcnt lgkmcnt(6)
	v_mfma_f32_32x32x16_bf16 v[50:65], v[22:25], v[198:201], v[50:65]
	ds_read_b64_tr_b16 v[236:237], v131 offset:5120
	ds_read_b64_tr_b16 v[238:239], v131 offset:7168
	v_max3_f32 v152, v152, v101, v102
	s_waitcnt lgkmcnt(6)
	v_mfma_f32_32x32x16_bf16 v[50:65], v[26:29], v[212:215], v[50:65]
	ds_read_b64_tr_b16 v[198:199], v131 offset:9216
	ds_read_b64_tr_b16 v[200:201], v131 offset:11264
	v_max3_f32 v174, v174, v117, v118
	s_waitcnt lgkmcnt(6)
	v_mfma_f32_32x32x16_bf16 v[50:65], v[30:33], v[216:219], v[50:65]
	ds_read_b64_tr_b16 v[212:213], v131 offset:13312
	ds_read_b64_tr_b16 v[214:215], v131 offset:15360
	v_max3_f32 v152, v152, v103, v104
	s_waitcnt lgkmcnt(6)
	v_mfma_f32_32x32x16_bf16 v[34:49], v[18:21], v[220:223], v[34:49]
	ds_read_b64_tr_b16 v[216:217], v131 offset:1536
	ds_read_b64_tr_b16 v[218:219], v131 offset:3584
	v_max3_f32 v174, v174, v119, v120
	s_waitcnt lgkmcnt(6)
	v_mfma_f32_32x32x16_bf16 v[34:49], v[22:25], v[236:239], v[34:49]
	ds_read_b64_tr_b16 v[220:221], v131 offset:5632
	ds_read_b64_tr_b16 v[222:223], v131 offset:7680
	v_max3_f32 v152, v152, v105, v106
	s_waitcnt lgkmcnt(6)
	v_mfma_f32_32x32x16_bf16 v[34:49], v[26:29], v[198:201], v[34:49]
	ds_read_b64_tr_b16 v[236:237], v131 offset:9728
	ds_read_b64_tr_b16 v[238:239], v131 offset:11776
	v_max3_f32 v174, v174, v121, v122
	s_waitcnt lgkmcnt(6)
	v_mfma_f32_32x32x16_bf16 v[34:49], v[30:33], v[212:215], v[34:49]
	ds_read_b64_tr_b16 v[198:199], v131 offset:13824
	ds_read_b64_tr_b16 v[200:201], v131 offset:15872
	v_max3_f32 v152, v152, v107, v108
	s_waitcnt lgkmcnt(6)
	v_mfma_f32_32x32x16_bf16 v[2:17], v[18:21], v[216:219], v[2:17]
	v_max3_f32 v174, v174, v123, v124
	s_min_u32 s14, s90, 0x7c
	s_lshl_b32 s14, s14, 17
	s_add_i32 s19, s14, 0x60000
	s_add_i32 s92, s36, 0xffff0000
	s_mov_b32 s14, s10
	s_mov_b32 s15, s11
	buffer_load_dwordx4 v[224:227], v171, s[8:11], s19 offen
	s_waitcnt lgkmcnt(4)
	v_mfma_f32_32x32x16_bf16 v[2:17], v[22:25], v[220:223], v[2:17]
	v_max3_f32 v152, v152, v109, v110
	buffer_load_dwordx4 v[228:231], v172, s[12:15], s92 offen
	s_waitcnt lgkmcnt(2)
	v_mfma_f32_32x32x16_bf16 v[2:17], v[26:29], v[236:239], v[2:17]
	v_max3_f32 v174, v174, v125, v126
	buffer_load_dwordx4 v[232:235], v172, s[12:15], s36 offen
	s_waitcnt lgkmcnt(0)
	v_mfma_f32_32x32x16_bf16 v[2:17], v[30:33], v[198:201], v[2:17]
	v_max3_f32 v152, v152, v111, v112
	v_mfma_f32_16x16x32_bf16 v[240:243], v[18:21], v[132:135], v[240:243]
	v_max3_f32 v174, v174, v127, v128
	v_mfma_f32_16x16x32_bf16 v[240:243], v[22:25], v[132:135], v[240:243]
	v_max_f32 v152, v152, v113
	v_mfma_f32_16x16x32_bf16 v[240:243], v[26:29], v[132:135], v[240:243]
	v_max_f32 v174, v174, v129
	v_mfma_f32_16x16x32_bf16 v[240:243], v[30:33], v[132:135], v[240:243]
	v_max_f32 v174, v174, v152
	s_setprio 0
	s_barrier
	s_add_i32 s36, s36, 0x20000
	s_add_i32 s90, s90, 1
	s_cmpk_eq_i32 s90, 0x7e
	s_cbranch_scc1 .Lu3_exit_b2_2
	s_branch .Lu3_b2_0
